# P6 gate-A and gate-B epilogues rewritten with batched loads (on top of P7 epilogue + mLSTM S^T hoist)
# speedup vs baseline: 1.0118x; 1.0020x over previous
; __device__ __forceinline__ unsigned pk2(float lo, float hi) { const f32x2 v = {lo, hi}; const bf16x2_t b = __builtin_convertvector(v, bf16x2_t); return __builtin_bit_cast(unsigned, b); }
; __device__ __forceinline__ float sigm(float x) { return __builtin_amdgcn_rcpf(1.f + __expf(-x)); }
;     __device__ __forceinline__ void operator()(const f32x4 (&acc)[2][2][4][2], const Unit& u, int wr, int wc, int fr, int fq) const {
;         const int row0 = u.pm * BM + wr * 64 + fr, col0 = u.pn * BM + wc * 32 + 8 * fq;
; #pragma unroll
;         for (int ai = 0; ai < 2; ++ai)
; #pragma unroll
;             for (int m = 0; m < 4; ++m) { const size_t r = (size_t)(row0 + ai * HALF + m * 16);
; #pragma unroll
;                 for (int bj = 0; bj < 2; ++bj) { const int c = col0 + bj * HALF;
;                     const v4u pg = *(const v4u*)(P + r * NINP + GTO + c); const f32x4 b0 = *(const f32x4*)(bg + c), b1 = *(const f32x4*)(bg + c + 4);
;                     f32x4 g0, g1;
;                     g0[0] = sigm(__uint_as_float(pg.x << 16) + b0[0]); g0[1] = sigm(__uint_as_float(pg.x & 0xffff0000u) + b0[1]);
;                     g0[2] = sigm(__uint_as_float(pg.y << 16) + b0[2]); g0[3] = sigm(__uint_as_float(pg.y & 0xffff0000u) + b0[3]);
;                     g1[0] = sigm(__uint_as_float(pg.z << 16) + b1[0]); g1[1] = sigm(__uint_as_float(pg.z & 0xffff0000u) + b1[1]);
;                     g1[2] = sigm(__uint_as_float(pg.w << 16) + b1[2]); g1[3] = sigm(__uint_as_float(pg.w & 0xffff0000u) + b1[3]);
;                     const f32x4 t0 = g0 * acc[ai][bj][m][0], t1 = g1 * acc[ai][bj][m][1]; v4u tw; tw.x = pk2(t0[0], t0[1]); tw.y = pk2(t0[2], t0[3]); tw.z = pk2(t1[0], t1[1]); tw.w = pk2(t1[2], t1[3]);
;                     *(v4u*)(TMP + r * D + c) = tw; } }
;     }
.LBB0_1261:
	v_lshl_add_u32 v152, s2, 8, v165
	v_lshl_or_b32 v150, s3, 8, v167
	v_mov_b64_e32 v[154:155], s[10:11]
	v_mad_i64_i32 v[146:147], s[2:3], v152, s52, v[154:155]
	v_ashrrev_i32_e32 v151, 31, v150
	v_lshl_add_u64 v[146:147], v[146:147], 0, s[18:19]
	v_lshlrev_b64 v[148:149], 1, v[150:151]
	v_readlane_b32 s56, v237, 0
	v_readlane_b32 s62, v237, 6
	v_readlane_b32 s63, v237, 7
	v_readlane_b32 s57, v237, 1
	v_readlane_b32 s58, v237, 2
	v_readlane_b32 s59, v237, 3
	v_readlane_b32 s60, v237, 4
	v_readlane_b32 s61, v237, 5
	v_readlane_b32 s64, v237, 8
	v_readlane_b32 s65, v237, 9
	v_readlane_b32 s66, v237, 10
	v_readlane_b32 s67, v237, 11
	v_readlane_b32 s68, v237, 12
	v_readlane_b32 s69, v237, 13
	v_readlane_b32 s70, v237, 14
	v_readlane_b32 s71, v237, 15
	v_lshl_add_u64 v[146:147], v[146:147], 0, v[148:149]
	v_ashrrev_i32_e32 v153, 31, v152
	v_lshlrev_b64 v[238:239], 12, v[152:153]
	v_lshl_add_u64 v[238:239], s[8:9], 0, v[238:239]
	v_lshl_add_u64 v[238:239], v[238:239], 0, v[148:149]
	v_lshl_add_u64 v[240:241], v[150:151], 2, s[62:63]
	s_andn2_b64 vcc, exec, s[4:5]
	s_lshl_b32 s98, s52, 4
	s_mov_b32 s99, 0
	s_mov_b32 s100, 0x10000
	s_mov_b32 s101, 0
	global_load_dwordx4 v[204:207], v[240:241], off
	global_load_dwordx4 v[208:211], v[240:241], off offset:16
	global_load_dwordx4 v[212:215], v[240:241], off offset:512
	global_load_dwordx4 v[216:219], v[240:241], off offset:528
	v_lshl_add_u64 v[242:243], s[98:99], 3, v[146:147]
	v_lshl_add_u64 v[154:155], s[100:101], 3, v[238:239]
	global_load_dwordx4 v[172:175], v[146:147], off
	global_load_dwordx4 v[176:179], v[146:147], off offset:256
	v_lshl_add_u64 v[146:147], v[146:147], 0, s[98:99]
	global_load_dwordx4 v[180:183], v[146:147], off
	global_load_dwordx4 v[184:187], v[146:147], off offset:256
	v_lshl_add_u64 v[146:147], v[146:147], 0, s[98:99]
	global_load_dwordx4 v[188:191], v[146:147], off
	global_load_dwordx4 v[192:195], v[146:147], off offset:256
	v_lshl_add_u64 v[146:147], v[146:147], 0, s[98:99]
	global_load_dwordx4 v[196:199], v[146:147], off
	global_load_dwordx4 v[200:203], v[146:147], off offset:256
	s_waitcnt vmcnt(0)
	v_lshlrev_b32_e32 v220, 16, v172
	v_and_b32_e32 v221, 0xffff0000, v172
	v_lshlrev_b32_e32 v222, 16, v173
	v_and_b32_e32 v223, 0xffff0000, v173
	v_lshlrev_b32_e32 v224, 16, v174
	v_and_b32_e32 v225, 0xffff0000, v174
	v_lshlrev_b32_e32 v226, 16, v175
	v_and_b32_e32 v227, 0xffff0000, v175
	v_add_f32_e32 v220, v204, v220
	v_add_f32_e32 v221, v205, v221
	v_add_f32_e32 v222, v206, v222
	v_add_f32_e32 v223, v207, v223
	v_add_f32_e32 v224, v208, v224
	v_add_f32_e32 v225, v209, v225
	v_add_f32_e32 v226, v210, v226
	v_add_f32_e32 v227, v211, v227
	v_mul_f32_e32 v220, 0xbfb8aa3b, v220
	v_mul_f32_e32 v221, 0xbfb8aa3b, v221
	v_mul_f32_e32 v222, 0xbfb8aa3b, v222
	v_mul_f32_e32 v223, 0xbfb8aa3b, v223
	v_mul_f32_e32 v224, 0xbfb8aa3b, v224
	v_mul_f32_e32 v225, 0xbfb8aa3b, v225
	v_mul_f32_e32 v226, 0xbfb8aa3b, v226
	v_mul_f32_e32 v227, 0xbfb8aa3b, v227
	v_exp_f32_e32 v220, v220
	v_exp_f32_e32 v221, v221
	v_exp_f32_e32 v222, v222
	v_exp_f32_e32 v223, v223
	v_exp_f32_e32 v224, v224
	v_exp_f32_e32 v225, v225
	v_exp_f32_e32 v226, v226
	v_exp_f32_e32 v227, v227
	v_add_f32_e32 v220, 1.0, v220
	v_add_f32_e32 v221, 1.0, v221
	v_add_f32_e32 v222, 1.0, v222
	v_add_f32_e32 v223, 1.0, v223
	v_add_f32_e32 v224, 1.0, v224
	v_add_f32_e32 v225, 1.0, v225
	v_add_f32_e32 v226, 1.0, v226
	v_add_f32_e32 v227, 1.0, v227
	v_rcp_f32_e32 v220, v220
	v_rcp_f32_e32 v221, v221
	v_rcp_f32_e32 v222, v222
	v_rcp_f32_e32 v223, v223
	v_rcp_f32_e32 v224, v224
	v_rcp_f32_e32 v225, v225
	v_rcp_f32_e32 v226, v226
	v_rcp_f32_e32 v227, v227
	v_pk_mul_f32 v[126:127], v[126:127], v[220:221]
	v_pk_mul_f32 v[128:129], v[128:129], v[222:223]
	v_pk_mul_f32 v[122:123], v[122:123], v[224:225]
	v_pk_mul_f32 v[124:125], v[124:125], v[226:227]
	v_cvt_pk_bf16_f32 v220, v126, v127
	v_cvt_pk_bf16_f32 v221, v128, v129
	v_cvt_pk_bf16_f32 v222, v122, v123
	v_cvt_pk_bf16_f32 v223, v124, v125
	global_store_dwordx4 v[238:239], v[220:223], off
	v_lshlrev_b32_e32 v228, 16, v176
	v_and_b32_e32 v229, 0xffff0000, v176
	v_lshlrev_b32_e32 v230, 16, v177
	v_and_b32_e32 v231, 0xffff0000, v177
	v_lshlrev_b32_e32 v232, 16, v178
	v_and_b32_e32 v233, 0xffff0000, v178
	v_lshlrev_b32_e32 v234, 16, v179
	v_and_b32_e32 v235, 0xffff0000, v179
	v_add_f32_e32 v228, v212, v228
	v_add_f32_e32 v229, v213, v229
	v_add_f32_e32 v230, v214, v230
	v_add_f32_e32 v231, v215, v231
	v_add_f32_e32 v232, v216, v232
	v_add_f32_e32 v233, v217, v233
	v_add_f32_e32 v234, v218, v234
	v_add_f32_e32 v235, v219, v235
	v_mul_f32_e32 v228, 0xbfb8aa3b, v228
	v_mul_f32_e32 v229, 0xbfb8aa3b, v229
	v_mul_f32_e32 v230, 0xbfb8aa3b, v230
	v_mul_f32_e32 v231, 0xbfb8aa3b, v231
	v_mul_f32_e32 v232, 0xbfb8aa3b, v232
	v_mul_f32_e32 v233, 0xbfb8aa3b, v233
	v_mul_f32_e32 v234, 0xbfb8aa3b, v234
	v_mul_f32_e32 v235, 0xbfb8aa3b, v235
	v_exp_f32_e32 v228, v228
	v_exp_f32_e32 v229, v229
	v_exp_f32_e32 v230, v230
	v_exp_f32_e32 v231, v231
	v_exp_f32_e32 v232, v232
	v_exp_f32_e32 v233, v233
	v_exp_f32_e32 v234, v234
	v_exp_f32_e32 v235, v235
	v_add_f32_e32 v228, 1.0, v228
	v_add_f32_e32 v229, 1.0, v229
	v_add_f32_e32 v230, 1.0, v230
	v_add_f32_e32 v231, 1.0, v231
	v_add_f32_e32 v232, 1.0, v232
	v_add_f32_e32 v233, 1.0, v233
	v_add_f32_e32 v234, 1.0, v234
	v_add_f32_e32 v235, 1.0, v235
	v_rcp_f32_e32 v228, v228
	v_rcp_f32_e32 v229, v229
	v_rcp_f32_e32 v230, v230
	v_rcp_f32_e32 v231, v231
	v_rcp_f32_e32 v232, v232
	v_rcp_f32_e32 v233, v233
	v_rcp_f32_e32 v234, v234
	v_rcp_f32_e32 v235, v235
	v_pk_mul_f32 v[118:119], v[118:119], v[228:229]
	v_pk_mul_f32 v[120:121], v[120:121], v[230:231]
; __device__ __forceinline__ unsigned pk2(float lo, float hi) { const f32x2 v = {lo, hi}; const bf16x2_t b = __builtin_convertvector(v, bf16x2_t); return __builtin_bit_cast(unsigned, b); }
; __device__ __forceinline__ float sigm(float x) { return __builtin_amdgcn_rcpf(1.f + __expf(-x)); }
;     __device__ __forceinline__ void operator()(const f32x4 (&acc)[2][2][4][2], const Unit& u, int wr, int wc, int fr, int fq) const {
;         const int row0 = u.pm * BM + wr * 64 + fr, col0 = u.pn * BM + wc * 32 + 8 * fq;
; #pragma unroll
;         for (int ai = 0; ai < 2; ++ai)
; #pragma unroll
;             for (int m = 0; m < 4; ++m) { const size_t r = (size_t)(row0 + ai * HALF + m * 16);
; #pragma unroll
;                 for (int bj = 0; bj < 2; ++bj) { const int c = col0 + bj * HALF;
;                     const v4u pg = *(const v4u*)(P + r * NINP + GTO + c); const f32x4 b0 = *(const f32x4*)(bg + c), b1 = *(const f32x4*)(bg + c + 4);
;                     f32x4 g0, g1;
;                     g0[0] = sigm(__uint_as_float(pg.x << 16) + b0[0]); g0[1] = sigm(__uint_as_float(pg.x & 0xffff0000u) + b0[1]);
;                     g0[2] = sigm(__uint_as_float(pg.y << 16) + b0[2]); g0[3] = sigm(__uint_as_float(pg.y & 0xffff0000u) + b0[3]);
;                     g1[0] = sigm(__uint_as_float(pg.z << 16) + b1[0]); g1[1] = sigm(__uint_as_float(pg.z & 0xffff0000u) + b1[1]);
;                     g1[2] = sigm(__uint_as_float(pg.w << 16) + b1[2]); g1[3] = sigm(__uint_as_float(pg.w & 0xffff0000u) + b1[3]);
;                     const f32x4 t0 = g0 * acc[ai][bj][m][0], t1 = g1 * acc[ai][bj][m][1]; v4u tw; tw.x = pk2(t0[0], t0[1]); tw.y = pk2(t0[2], t0[3]); tw.z = pk2(t1[0], t1[1]); tw.w = pk2(t1[2], t1[3]);
;                     *(v4u*)(TMP + r * D + c) = tw; } }
;     }
	v_pk_mul_f32 v[114:115], v[114:115], v[232:233]
	v_pk_mul_f32 v[116:117], v[116:117], v[234:235]
	v_cvt_pk_bf16_f32 v228, v118, v119
	v_cvt_pk_bf16_f32 v229, v120, v121
	v_cvt_pk_bf16_f32 v230, v114, v115
	v_cvt_pk_bf16_f32 v231, v116, v117
	global_store_dwordx4 v[238:239], v[228:231], off offset:256
	v_lshl_add_u64 v[238:239], v[238:239], 0, s[100:101]
	v_lshlrev_b32_e32 v220, 16, v180
	v_and_b32_e32 v221, 0xffff0000, v180
	v_lshlrev_b32_e32 v222, 16, v181
	v_and_b32_e32 v223, 0xffff0000, v181
	v_lshlrev_b32_e32 v224, 16, v182
	v_and_b32_e32 v225, 0xffff0000, v182
	v_lshlrev_b32_e32 v226, 16, v183
	v_and_b32_e32 v227, 0xffff0000, v183
	v_add_f32_e32 v220, v204, v220
	v_add_f32_e32 v221, v205, v221
	v_add_f32_e32 v222, v206, v222
	v_add_f32_e32 v223, v207, v223
	v_add_f32_e32 v224, v208, v224
	v_add_f32_e32 v225, v209, v225
	v_add_f32_e32 v226, v210, v226
	v_add_f32_e32 v227, v211, v227
	v_mul_f32_e32 v220, 0xbfb8aa3b, v220
	v_mul_f32_e32 v221, 0xbfb8aa3b, v221
	v_mul_f32_e32 v222, 0xbfb8aa3b, v222
	v_mul_f32_e32 v223, 0xbfb8aa3b, v223
	v_mul_f32_e32 v224, 0xbfb8aa3b, v224
	v_mul_f32_e32 v225, 0xbfb8aa3b, v225
	v_mul_f32_e32 v226, 0xbfb8aa3b, v226
	v_mul_f32_e32 v227, 0xbfb8aa3b, v227
	v_exp_f32_e32 v220, v220
	v_exp_f32_e32 v221, v221
	v_exp_f32_e32 v222, v222
	v_exp_f32_e32 v223, v223
	v_exp_f32_e32 v224, v224
	v_exp_f32_e32 v225, v225
	v_exp_f32_e32 v226, v226
	v_exp_f32_e32 v227, v227
	v_add_f32_e32 v220, 1.0, v220
	v_add_f32_e32 v221, 1.0, v221
	v_add_f32_e32 v222, 1.0, v222
	v_add_f32_e32 v223, 1.0, v223
	v_add_f32_e32 v224, 1.0, v224
	v_add_f32_e32 v225, 1.0, v225
	v_add_f32_e32 v226, 1.0, v226
	v_add_f32_e32 v227, 1.0, v227
	v_rcp_f32_e32 v220, v220
	v_rcp_f32_e32 v221, v221
	v_rcp_f32_e32 v222, v222
	v_rcp_f32_e32 v223, v223
	v_rcp_f32_e32 v224, v224
	v_rcp_f32_e32 v225, v225
	v_rcp_f32_e32 v226, v226
	v_rcp_f32_e32 v227, v227
	v_pk_mul_f32 v[110:111], v[110:111], v[220:221]
	v_pk_mul_f32 v[112:113], v[112:113], v[222:223]
	v_pk_mul_f32 v[106:107], v[106:107], v[224:225]
	v_pk_mul_f32 v[108:109], v[108:109], v[226:227]
	v_cvt_pk_bf16_f32 v220, v110, v111
	v_cvt_pk_bf16_f32 v221, v112, v113
	v_cvt_pk_bf16_f32 v222, v106, v107
	v_cvt_pk_bf16_f32 v223, v108, v109
	global_store_dwordx4 v[238:239], v[220:223], off
	v_lshlrev_b32_e32 v228, 16, v184
	v_and_b32_e32 v229, 0xffff0000, v184
	v_lshlrev_b32_e32 v230, 16, v185
	v_and_b32_e32 v231, 0xffff0000, v185
	v_lshlrev_b32_e32 v232, 16, v186
	v_and_b32_e32 v233, 0xffff0000, v186
	v_lshlrev_b32_e32 v234, 16, v187
	v_and_b32_e32 v235, 0xffff0000, v187
	v_add_f32_e32 v228, v212, v228
	v_add_f32_e32 v229, v213, v229
	v_add_f32_e32 v230, v214, v230
	v_add_f32_e32 v231, v215, v231
	v_add_f32_e32 v232, v216, v232
	v_add_f32_e32 v233, v217, v233
	v_add_f32_e32 v234, v218, v234
	v_add_f32_e32 v235, v219, v235
	v_mul_f32_e32 v228, 0xbfb8aa3b, v228
	v_mul_f32_e32 v229, 0xbfb8aa3b, v229
	v_mul_f32_e32 v230, 0xbfb8aa3b, v230
	v_mul_f32_e32 v231, 0xbfb8aa3b, v231
	v_mul_f32_e32 v232, 0xbfb8aa3b, v232
	v_mul_f32_e32 v233, 0xbfb8aa3b, v233
	v_mul_f32_e32 v234, 0xbfb8aa3b, v234
	v_mul_f32_e32 v235, 0xbfb8aa3b, v235
	v_exp_f32_e32 v228, v228
	v_exp_f32_e32 v229, v229
	v_exp_f32_e32 v230, v230
	v_exp_f32_e32 v231, v231
	v_exp_f32_e32 v232, v232
	v_exp_f32_e32 v233, v233
	v_exp_f32_e32 v234, v234
	v_exp_f32_e32 v235, v235
	v_add_f32_e32 v228, 1.0, v228
	v_add_f32_e32 v229, 1.0, v229
	v_add_f32_e32 v230, 1.0, v230
	v_add_f32_e32 v231, 1.0, v231
	v_add_f32_e32 v232, 1.0, v232
	v_add_f32_e32 v233, 1.0, v233
	v_add_f32_e32 v234, 1.0, v234
	v_add_f32_e32 v235, 1.0, v235
	v_rcp_f32_e32 v228, v228
	v_rcp_f32_e32 v229, v229
	v_rcp_f32_e32 v230, v230
	v_rcp_f32_e32 v231, v231
	v_rcp_f32_e32 v232, v232
	v_rcp_f32_e32 v233, v233
	v_rcp_f32_e32 v234, v234
	v_rcp_f32_e32 v235, v235
	v_pk_mul_f32 v[102:103], v[102:103], v[228:229]
	v_pk_mul_f32 v[104:105], v[104:105], v[230:231]
	v_pk_mul_f32 v[98:99], v[98:99], v[232:233]
	v_pk_mul_f32 v[100:101], v[100:101], v[234:235]
	v_cvt_pk_bf16_f32 v228, v102, v103
	v_cvt_pk_bf16_f32 v229, v104, v105
	v_cvt_pk_bf16_f32 v230, v98, v99
	v_cvt_pk_bf16_f32 v231, v100, v101
	global_store_dwordx4 v[238:239], v[228:231], off offset:256
	v_lshl_add_u64 v[238:239], v[238:239], 0, s[100:101]
	v_lshlrev_b32_e32 v220, 16, v188
	v_and_b32_e32 v221, 0xffff0000, v188
	v_lshlrev_b32_e32 v222, 16, v189
	v_and_b32_e32 v223, 0xffff0000, v189
	v_lshlrev_b32_e32 v224, 16, v190
	v_and_b32_e32 v225, 0xffff0000, v190
	v_lshlrev_b32_e32 v226, 16, v191
	v_and_b32_e32 v227, 0xffff0000, v191
	v_add_f32_e32 v220, v204, v220
	v_add_f32_e32 v221, v205, v221
	v_add_f32_e32 v222, v206, v222
	v_add_f32_e32 v223, v207, v223
	v_add_f32_e32 v224, v208, v224
	v_add_f32_e32 v225, v209, v225
	v_add_f32_e32 v226, v210, v226
	v_add_f32_e32 v227, v211, v227
	v_mul_f32_e32 v220, 0xbfb8aa3b, v220
	v_mul_f32_e32 v221, 0xbfb8aa3b, v221
	v_mul_f32_e32 v222, 0xbfb8aa3b, v222
	v_mul_f32_e32 v223, 0xbfb8aa3b, v223
	v_mul_f32_e32 v224, 0xbfb8aa3b, v224
	v_mul_f32_e32 v225, 0xbfb8aa3b, v225
	v_mul_f32_e32 v226, 0xbfb8aa3b, v226
	v_mul_f32_e32 v227, 0xbfb8aa3b, v227
	v_exp_f32_e32 v220, v220
	v_exp_f32_e32 v221, v221
	v_exp_f32_e32 v222, v222
	v_exp_f32_e32 v223, v223
	v_exp_f32_e32 v224, v224
	v_exp_f32_e32 v225, v225
	v_exp_f32_e32 v226, v226
	v_exp_f32_e32 v227, v227
	v_add_f32_e32 v220, 1.0, v220
	v_add_f32_e32 v221, 1.0, v221
	v_add_f32_e32 v222, 1.0, v222
	v_add_f32_e32 v223, 1.0, v223
	v_add_f32_e32 v224, 1.0, v224
	v_add_f32_e32 v225, 1.0, v225
	v_add_f32_e32 v226, 1.0, v226
	v_add_f32_e32 v227, 1.0, v227
	v_rcp_f32_e32 v220, v220
	v_rcp_f32_e32 v221, v221
	v_rcp_f32_e32 v222, v222
	v_rcp_f32_e32 v223, v223
; __device__ __forceinline__ unsigned pk2(float lo, float hi) { const f32x2 v = {lo, hi}; const bf16x2_t b = __builtin_convertvector(v, bf16x2_t); return __builtin_bit_cast(unsigned, b); }
; __device__ __forceinline__ float sigm(float x) { return __builtin_amdgcn_rcpf(1.f + __expf(-x)); }
;     __device__ __forceinline__ void operator()(const f32x4 (&acc)[2][2][4][2], const Unit& u, int wr, int wc, int fr, int fq) const {
;         const int row0 = u.pm * BM + wr * 64 + fr, col0 = u.pn * BM + wc * 32 + 8 * fq;
; #pragma unroll
;         for (int ai = 0; ai < 2; ++ai)
; #pragma unroll
;             for (int m = 0; m < 4; ++m) { const size_t r = (size_t)(row0 + ai * HALF + m * 16);
; #pragma unroll
;                 for (int bj = 0; bj < 2; ++bj) { const int c = col0 + bj * HALF;
;                     const v4u pg = *(const v4u*)(P + r * NINP + GTO + c); const f32x4 b0 = *(const f32x4*)(bg + c), b1 = *(const f32x4*)(bg + c + 4);
;                     f32x4 g0, g1;
;                     g0[0] = sigm(__uint_as_float(pg.x << 16) + b0[0]); g0[1] = sigm(__uint_as_float(pg.x & 0xffff0000u) + b0[1]);
;                     g0[2] = sigm(__uint_as_float(pg.y << 16) + b0[2]); g0[3] = sigm(__uint_as_float(pg.y & 0xffff0000u) + b0[3]);
;                     g1[0] = sigm(__uint_as_float(pg.z << 16) + b1[0]); g1[1] = sigm(__uint_as_float(pg.z & 0xffff0000u) + b1[1]);
;                     g1[2] = sigm(__uint_as_float(pg.w << 16) + b1[2]); g1[3] = sigm(__uint_as_float(pg.w & 0xffff0000u) + b1[3]);
;                     const f32x4 t0 = g0 * acc[ai][bj][m][0], t1 = g1 * acc[ai][bj][m][1]; v4u tw; tw.x = pk2(t0[0], t0[1]); tw.y = pk2(t0[2], t0[3]); tw.z = pk2(t1[0], t1[1]); tw.w = pk2(t1[2], t1[3]);
;                     *(v4u*)(TMP + r * D + c) = tw; } }
;     }
	v_rcp_f32_e32 v224, v224
	v_rcp_f32_e32 v225, v225
	v_rcp_f32_e32 v226, v226
	v_rcp_f32_e32 v227, v227
	v_pk_mul_f32 v[94:95], v[94:95], v[220:221]
	v_pk_mul_f32 v[96:97], v[96:97], v[222:223]
	v_pk_mul_f32 v[90:91], v[90:91], v[224:225]
	v_pk_mul_f32 v[92:93], v[92:93], v[226:227]
	v_cvt_pk_bf16_f32 v220, v94, v95
	v_cvt_pk_bf16_f32 v221, v96, v97
	v_cvt_pk_bf16_f32 v222, v90, v91
	v_cvt_pk_bf16_f32 v223, v92, v93
	global_store_dwordx4 v[238:239], v[220:223], off
	v_lshlrev_b32_e32 v228, 16, v192
	v_and_b32_e32 v229, 0xffff0000, v192
	v_lshlrev_b32_e32 v230, 16, v193
	v_and_b32_e32 v231, 0xffff0000, v193
	v_lshlrev_b32_e32 v232, 16, v194
	v_and_b32_e32 v233, 0xffff0000, v194
	v_lshlrev_b32_e32 v234, 16, v195
	v_and_b32_e32 v235, 0xffff0000, v195
	v_add_f32_e32 v228, v212, v228
	v_add_f32_e32 v229, v213, v229
	v_add_f32_e32 v230, v214, v230
	v_add_f32_e32 v231, v215, v231
	v_add_f32_e32 v232, v216, v232
	v_add_f32_e32 v233, v217, v233
	v_add_f32_e32 v234, v218, v234
	v_add_f32_e32 v235, v219, v235
	v_mul_f32_e32 v228, 0xbfb8aa3b, v228
	v_mul_f32_e32 v229, 0xbfb8aa3b, v229
	v_mul_f32_e32 v230, 0xbfb8aa3b, v230
	v_mul_f32_e32 v231, 0xbfb8aa3b, v231
	v_mul_f32_e32 v232, 0xbfb8aa3b, v232
	v_mul_f32_e32 v233, 0xbfb8aa3b, v233
	v_mul_f32_e32 v234, 0xbfb8aa3b, v234
	v_mul_f32_e32 v235, 0xbfb8aa3b, v235
	v_exp_f32_e32 v228, v228
	v_exp_f32_e32 v229, v229
	v_exp_f32_e32 v230, v230
	v_exp_f32_e32 v231, v231
	v_exp_f32_e32 v232, v232
	v_exp_f32_e32 v233, v233
	v_exp_f32_e32 v234, v234
	v_exp_f32_e32 v235, v235
	v_add_f32_e32 v228, 1.0, v228
	v_add_f32_e32 v229, 1.0, v229
	v_add_f32_e32 v230, 1.0, v230
	v_add_f32_e32 v231, 1.0, v231
	v_add_f32_e32 v232, 1.0, v232
	v_add_f32_e32 v233, 1.0, v233
	v_add_f32_e32 v234, 1.0, v234
	v_add_f32_e32 v235, 1.0, v235
	v_rcp_f32_e32 v228, v228
	v_rcp_f32_e32 v229, v229
	v_rcp_f32_e32 v230, v230
	v_rcp_f32_e32 v231, v231
	v_rcp_f32_e32 v232, v232
	v_rcp_f32_e32 v233, v233
	v_rcp_f32_e32 v234, v234
	v_rcp_f32_e32 v235, v235
	v_pk_mul_f32 v[86:87], v[86:87], v[228:229]
	v_pk_mul_f32 v[88:89], v[88:89], v[230:231]
	v_pk_mul_f32 v[82:83], v[82:83], v[232:233]
	v_pk_mul_f32 v[84:85], v[84:85], v[234:235]
	v_cvt_pk_bf16_f32 v228, v86, v87
	v_cvt_pk_bf16_f32 v229, v88, v89
	v_cvt_pk_bf16_f32 v230, v82, v83
	v_cvt_pk_bf16_f32 v231, v84, v85
	global_store_dwordx4 v[238:239], v[228:231], off offset:256
	v_lshl_add_u64 v[238:239], v[238:239], 0, s[100:101]
	v_lshlrev_b32_e32 v220, 16, v196
	v_and_b32_e32 v221, 0xffff0000, v196
	v_lshlrev_b32_e32 v222, 16, v197
	v_and_b32_e32 v223, 0xffff0000, v197
	v_lshlrev_b32_e32 v224, 16, v198
	v_and_b32_e32 v225, 0xffff0000, v198
	v_lshlrev_b32_e32 v226, 16, v199
	v_and_b32_e32 v227, 0xffff0000, v199
	v_add_f32_e32 v220, v204, v220
	v_add_f32_e32 v221, v205, v221
	v_add_f32_e32 v222, v206, v222
	v_add_f32_e32 v223, v207, v223
	v_add_f32_e32 v224, v208, v224
	v_add_f32_e32 v225, v209, v225
	v_add_f32_e32 v226, v210, v226
	v_add_f32_e32 v227, v211, v227
	v_mul_f32_e32 v220, 0xbfb8aa3b, v220
	v_mul_f32_e32 v221, 0xbfb8aa3b, v221
	v_mul_f32_e32 v222, 0xbfb8aa3b, v222
	v_mul_f32_e32 v223, 0xbfb8aa3b, v223
	v_mul_f32_e32 v224, 0xbfb8aa3b, v224
	v_mul_f32_e32 v225, 0xbfb8aa3b, v225
	v_mul_f32_e32 v226, 0xbfb8aa3b, v226
	v_mul_f32_e32 v227, 0xbfb8aa3b, v227
	v_exp_f32_e32 v220, v220
	v_exp_f32_e32 v221, v221
	v_exp_f32_e32 v222, v222
	v_exp_f32_e32 v223, v223
	v_exp_f32_e32 v224, v224
	v_exp_f32_e32 v225, v225
	v_exp_f32_e32 v226, v226
	v_exp_f32_e32 v227, v227
	v_add_f32_e32 v220, 1.0, v220
	v_add_f32_e32 v221, 1.0, v221
	v_add_f32_e32 v222, 1.0, v222
	v_add_f32_e32 v223, 1.0, v223
	v_add_f32_e32 v224, 1.0, v224
	v_add_f32_e32 v225, 1.0, v225
	v_add_f32_e32 v226, 1.0, v226
	v_add_f32_e32 v227, 1.0, v227
	v_rcp_f32_e32 v220, v220
	v_rcp_f32_e32 v221, v221
	v_rcp_f32_e32 v222, v222
	v_rcp_f32_e32 v223, v223
	v_rcp_f32_e32 v224, v224
	v_rcp_f32_e32 v225, v225
	v_rcp_f32_e32 v226, v226
	v_rcp_f32_e32 v227, v227
	v_pk_mul_f32 v[78:79], v[78:79], v[220:221]
	v_pk_mul_f32 v[80:81], v[80:81], v[222:223]
	v_pk_mul_f32 v[74:75], v[74:75], v[224:225]
	v_pk_mul_f32 v[76:77], v[76:77], v[226:227]
	v_cvt_pk_bf16_f32 v220, v78, v79
	v_cvt_pk_bf16_f32 v221, v80, v81
	v_cvt_pk_bf16_f32 v222, v74, v75
	v_cvt_pk_bf16_f32 v223, v76, v77
	global_store_dwordx4 v[238:239], v[220:223], off
	v_lshlrev_b32_e32 v228, 16, v200
	v_and_b32_e32 v229, 0xffff0000, v200
	v_lshlrev_b32_e32 v230, 16, v201
	v_and_b32_e32 v231, 0xffff0000, v201
	v_lshlrev_b32_e32 v232, 16, v202
	v_and_b32_e32 v233, 0xffff0000, v202
	v_lshlrev_b32_e32 v234, 16, v203
	v_and_b32_e32 v235, 0xffff0000, v203
	v_add_f32_e32 v228, v212, v228
	v_add_f32_e32 v229, v213, v229
	v_add_f32_e32 v230, v214, v230
	v_add_f32_e32 v231, v215, v231
	v_add_f32_e32 v232, v216, v232
	v_add_f32_e32 v233, v217, v233
	v_add_f32_e32 v234, v218, v234
	v_add_f32_e32 v235, v219, v235
	v_mul_f32_e32 v228, 0xbfb8aa3b, v228
	v_mul_f32_e32 v229, 0xbfb8aa3b, v229
	v_mul_f32_e32 v230, 0xbfb8aa3b, v230
	v_mul_f32_e32 v231, 0xbfb8aa3b, v231
	v_mul_f32_e32 v232, 0xbfb8aa3b, v232
	v_mul_f32_e32 v233, 0xbfb8aa3b, v233
	v_mul_f32_e32 v234, 0xbfb8aa3b, v234
	v_mul_f32_e32 v235, 0xbfb8aa3b, v235
	v_exp_f32_e32 v228, v228
	v_exp_f32_e32 v229, v229
	v_exp_f32_e32 v230, v230
	v_exp_f32_e32 v231, v231
	v_exp_f32_e32 v232, v232
	v_exp_f32_e32 v233, v233
	v_exp_f32_e32 v234, v234
	v_exp_f32_e32 v235, v235
	v_add_f32_e32 v228, 1.0, v228
	v_add_f32_e32 v229, 1.0, v229
	v_add_f32_e32 v230, 1.0, v230
	v_add_f32_e32 v231, 1.0, v231
	v_add_f32_e32 v232, 1.0, v232
	v_add_f32_e32 v233, 1.0, v233
	v_add_f32_e32 v234, 1.0, v234
	v_add_f32_e32 v235, 1.0, v235
	v_rcp_f32_e32 v228, v228
	v_rcp_f32_e32 v229, v229
	v_rcp_f32_e32 v230, v230
	v_rcp_f32_e32 v231, v231
	v_rcp_f32_e32 v232, v232
	v_rcp_f32_e32 v233, v233
	v_rcp_f32_e32 v234, v234
	v_rcp_f32_e32 v235, v235
	v_pk_mul_f32 v[70:71], v[70:71], v[228:229]
	v_pk_mul_f32 v[72:73], v[72:73], v[230:231]
	v_pk_mul_f32 v[66:67], v[66:67], v[232:233]
	v_pk_mul_f32 v[68:69], v[68:69], v[234:235]
	v_cvt_pk_bf16_f32 v228, v70, v71
	v_cvt_pk_bf16_f32 v229, v72, v73
	v_cvt_pk_bf16_f32 v230, v66, v67
	v_cvt_pk_bf16_f32 v231, v68, v69
	global_store_dwordx4 v[238:239], v[228:231], off offset:256
	global_load_dwordx4 v[122:125], v[242:243], off
	global_load_dwordx4 v[114:117], v[242:243], off offset:256
	v_lshl_add_u64 v[242:243], v[242:243], 0, s[98:99]
	global_load_dwordx4 v[106:109], v[242:243], off
	global_load_dwordx4 v[98:101], v[242:243], off offset:256
	v_lshl_add_u64 v[242:243], v[242:243], 0, s[98:99]
	global_load_dwordx4 v[90:93], v[242:243], off
	global_load_dwordx4 v[82:85], v[242:243], off offset:256
	v_lshl_add_u64 v[242:243], v[242:243], 0, s[98:99]
	global_load_dwordx4 v[74:77], v[242:243], off
	global_load_dwordx4 v[66:69], v[242:243], off offset:256
	s_waitcnt vmcnt(0)
; __device__ __forceinline__ unsigned pk2(float lo, float hi) { const f32x2 v = {lo, hi}; const bf16x2_t b = __builtin_convertvector(v, bf16x2_t); return __builtin_bit_cast(unsigned, b); }
; __device__ __forceinline__ float sigm(float x) { return __builtin_amdgcn_rcpf(1.f + __expf(-x)); }
;     __device__ __forceinline__ void operator()(const f32x4 (&acc)[2][2][4][2], const Unit& u, int wr, int wc, int fr, int fq) const {
;         const int row0 = u.pm * BM + wr * 64 + fr, col0 = u.pn * BM + wc * 32 + 8 * fq;
; #pragma unroll
;         for (int ai = 0; ai < 2; ++ai)
; #pragma unroll
;             for (int m = 0; m < 4; ++m) { const size_t r = (size_t)(row0 + ai * HALF + m * 16);
; #pragma unroll
;                 for (int bj = 0; bj < 2; ++bj) { const int c = col0 + bj * HALF;
;                     const v4u pg = *(const v4u*)(P + r * NINP + GTO + c); const f32x4 b0 = *(const f32x4*)(bg + c), b1 = *(const f32x4*)(bg + c + 4);
;                     f32x4 g0, g1;
;                     g0[0] = sigm(__uint_as_float(pg.x << 16) + b0[0]); g0[1] = sigm(__uint_as_float(pg.x & 0xffff0000u) + b0[1]);
;                     g0[2] = sigm(__uint_as_float(pg.y << 16) + b0[2]); g0[3] = sigm(__uint_as_float(pg.y & 0xffff0000u) + b0[3]);
;                     g1[0] = sigm(__uint_as_float(pg.z << 16) + b1[0]); g1[1] = sigm(__uint_as_float(pg.z & 0xffff0000u) + b1[1]);
;                     g1[2] = sigm(__uint_as_float(pg.w << 16) + b1[2]); g1[3] = sigm(__uint_as_float(pg.w & 0xffff0000u) + b1[3]);
;                     const f32x4 t0 = g0 * acc[ai][bj][m][0], t1 = g1 * acc[ai][bj][m][1]; v4u tw; tw.x = pk2(t0[0], t0[1]); tw.y = pk2(t0[2], t0[3]); tw.z = pk2(t1[0], t1[1]); tw.w = pk2(t1[2], t1[3]);
;                     *(v4u*)(TMP + r * D + c) = tw; } }
;     }
	v_lshlrev_b32_e32 v220, 16, v122
	v_and_b32_e32 v221, 0xffff0000, v122
	v_lshlrev_b32_e32 v222, 16, v123
	v_and_b32_e32 v223, 0xffff0000, v123
	v_lshlrev_b32_e32 v224, 16, v124
	v_and_b32_e32 v225, 0xffff0000, v124
	v_lshlrev_b32_e32 v226, 16, v125
	v_and_b32_e32 v227, 0xffff0000, v125
	v_add_f32_e32 v220, v204, v220
	v_add_f32_e32 v221, v205, v221
	v_add_f32_e32 v222, v206, v222
	v_add_f32_e32 v223, v207, v223
	v_add_f32_e32 v224, v208, v224
	v_add_f32_e32 v225, v209, v225
	v_add_f32_e32 v226, v210, v226
	v_add_f32_e32 v227, v211, v227
	v_mul_f32_e32 v220, 0xbfb8aa3b, v220
	v_mul_f32_e32 v221, 0xbfb8aa3b, v221
	v_mul_f32_e32 v222, 0xbfb8aa3b, v222
	v_mul_f32_e32 v223, 0xbfb8aa3b, v223
	v_mul_f32_e32 v224, 0xbfb8aa3b, v224
	v_mul_f32_e32 v225, 0xbfb8aa3b, v225
	v_mul_f32_e32 v226, 0xbfb8aa3b, v226
	v_mul_f32_e32 v227, 0xbfb8aa3b, v227
	v_exp_f32_e32 v220, v220
	v_exp_f32_e32 v221, v221
	v_exp_f32_e32 v222, v222
	v_exp_f32_e32 v223, v223
	v_exp_f32_e32 v224, v224
	v_exp_f32_e32 v225, v225
	v_exp_f32_e32 v226, v226
	v_exp_f32_e32 v227, v227
	v_add_f32_e32 v220, 1.0, v220
	v_add_f32_e32 v221, 1.0, v221
	v_add_f32_e32 v222, 1.0, v222
	v_add_f32_e32 v223, 1.0, v223
	v_add_f32_e32 v224, 1.0, v224
	v_add_f32_e32 v225, 1.0, v225
	v_add_f32_e32 v226, 1.0, v226
	v_add_f32_e32 v227, 1.0, v227
	v_rcp_f32_e32 v220, v220
	v_rcp_f32_e32 v221, v221
	v_rcp_f32_e32 v222, v222
	v_rcp_f32_e32 v223, v223
	v_rcp_f32_e32 v224, v224
	v_rcp_f32_e32 v225, v225
	v_rcp_f32_e32 v226, v226
	v_rcp_f32_e32 v227, v227
	v_pk_mul_f32 v[62:63], v[62:63], v[220:221]
	v_pk_mul_f32 v[64:65], v[64:65], v[222:223]
	v_pk_mul_f32 v[58:59], v[58:59], v[224:225]
	v_pk_mul_f32 v[60:61], v[60:61], v[226:227]
	v_cvt_pk_bf16_f32 v220, v62, v63
	v_cvt_pk_bf16_f32 v221, v64, v65
	v_cvt_pk_bf16_f32 v222, v58, v59
	v_cvt_pk_bf16_f32 v223, v60, v61
	global_store_dwordx4 v[154:155], v[220:223], off
	v_lshlrev_b32_e32 v228, 16, v114
	v_and_b32_e32 v229, 0xffff0000, v114
	v_lshlrev_b32_e32 v230, 16, v115
	v_and_b32_e32 v231, 0xffff0000, v115
	v_lshlrev_b32_e32 v232, 16, v116
	v_and_b32_e32 v233, 0xffff0000, v116
	v_lshlrev_b32_e32 v234, 16, v117
	v_and_b32_e32 v235, 0xffff0000, v117
	v_add_f32_e32 v228, v212, v228
	v_add_f32_e32 v229, v213, v229
	v_add_f32_e32 v230, v214, v230
	v_add_f32_e32 v231, v215, v231
	v_add_f32_e32 v232, v216, v232
	v_add_f32_e32 v233, v217, v233
	v_add_f32_e32 v234, v218, v234
	v_add_f32_e32 v235, v219, v235
	v_mul_f32_e32 v228, 0xbfb8aa3b, v228
	v_mul_f32_e32 v229, 0xbfb8aa3b, v229
	v_mul_f32_e32 v230, 0xbfb8aa3b, v230
	v_mul_f32_e32 v231, 0xbfb8aa3b, v231
	v_mul_f32_e32 v232, 0xbfb8aa3b, v232
	v_mul_f32_e32 v233, 0xbfb8aa3b, v233
	v_mul_f32_e32 v234, 0xbfb8aa3b, v234
	v_mul_f32_e32 v235, 0xbfb8aa3b, v235
	v_exp_f32_e32 v228, v228
	v_exp_f32_e32 v229, v229
	v_exp_f32_e32 v230, v230
	v_exp_f32_e32 v231, v231
	v_exp_f32_e32 v232, v232
	v_exp_f32_e32 v233, v233
	v_exp_f32_e32 v234, v234
	v_exp_f32_e32 v235, v235
	v_add_f32_e32 v228, 1.0, v228
	v_add_f32_e32 v229, 1.0, v229
	v_add_f32_e32 v230, 1.0, v230
	v_add_f32_e32 v231, 1.0, v231
	v_add_f32_e32 v232, 1.0, v232
	v_add_f32_e32 v233, 1.0, v233
	v_add_f32_e32 v234, 1.0, v234
	v_add_f32_e32 v235, 1.0, v235
	v_rcp_f32_e32 v228, v228
	v_rcp_f32_e32 v229, v229
	v_rcp_f32_e32 v230, v230
	v_rcp_f32_e32 v231, v231
	v_rcp_f32_e32 v232, v232
	v_rcp_f32_e32 v233, v233
	v_rcp_f32_e32 v234, v234
	v_rcp_f32_e32 v235, v235
	v_pk_mul_f32 v[54:55], v[54:55], v[228:229]
	v_pk_mul_f32 v[56:57], v[56:57], v[230:231]
	v_pk_mul_f32 v[50:51], v[50:51], v[232:233]
	v_pk_mul_f32 v[52:53], v[52:53], v[234:235]
	v_cvt_pk_bf16_f32 v228, v54, v55
	v_cvt_pk_bf16_f32 v229, v56, v57
	v_cvt_pk_bf16_f32 v230, v50, v51
	v_cvt_pk_bf16_f32 v231, v52, v53
	global_store_dwordx4 v[154:155], v[228:231], off offset:256
	v_lshl_add_u64 v[154:155], v[154:155], 0, s[100:101]
	v_lshlrev_b32_e32 v220, 16, v106
	v_and_b32_e32 v221, 0xffff0000, v106
	v_lshlrev_b32_e32 v222, 16, v107
	v_and_b32_e32 v223, 0xffff0000, v107
	v_lshlrev_b32_e32 v224, 16, v108
	v_and_b32_e32 v225, 0xffff0000, v108
	v_lshlrev_b32_e32 v226, 16, v109
	v_and_b32_e32 v227, 0xffff0000, v109
	v_add_f32_e32 v220, v204, v220
	v_add_f32_e32 v221, v205, v221
	v_add_f32_e32 v222, v206, v222
	v_add_f32_e32 v223, v207, v223
	v_add_f32_e32 v224, v208, v224
	v_add_f32_e32 v225, v209, v225
	v_add_f32_e32 v226, v210, v226
	v_add_f32_e32 v227, v211, v227
	v_mul_f32_e32 v220, 0xbfb8aa3b, v220
	v_mul_f32_e32 v221, 0xbfb8aa3b, v221
	v_mul_f32_e32 v222, 0xbfb8aa3b, v222
	v_mul_f32_e32 v223, 0xbfb8aa3b, v223
	v_mul_f32_e32 v224, 0xbfb8aa3b, v224
	v_mul_f32_e32 v225, 0xbfb8aa3b, v225
	v_mul_f32_e32 v226, 0xbfb8aa3b, v226
	v_mul_f32_e32 v227, 0xbfb8aa3b, v227
	v_exp_f32_e32 v220, v220
	v_exp_f32_e32 v221, v221
	v_exp_f32_e32 v222, v222
	v_exp_f32_e32 v223, v223
	v_exp_f32_e32 v224, v224
	v_exp_f32_e32 v225, v225
	v_exp_f32_e32 v226, v226
	v_exp_f32_e32 v227, v227
	v_add_f32_e32 v220, 1.0, v220
	v_add_f32_e32 v221, 1.0, v221
	v_add_f32_e32 v222, 1.0, v222
	v_add_f32_e32 v223, 1.0, v223
	v_add_f32_e32 v224, 1.0, v224
	v_add_f32_e32 v225, 1.0, v225
	v_add_f32_e32 v226, 1.0, v226
	v_add_f32_e32 v227, 1.0, v227
	v_rcp_f32_e32 v220, v220
	v_rcp_f32_e32 v221, v221
	v_rcp_f32_e32 v222, v222
	v_rcp_f32_e32 v223, v223
	v_rcp_f32_e32 v224, v224
	v_rcp_f32_e32 v225, v225
	v_rcp_f32_e32 v226, v226
	v_rcp_f32_e32 v227, v227
	v_pk_mul_f32 v[46:47], v[46:47], v[220:221]
	v_pk_mul_f32 v[48:49], v[48:49], v[222:223]
	v_pk_mul_f32 v[42:43], v[42:43], v[224:225]
	v_pk_mul_f32 v[44:45], v[44:45], v[226:227]
	v_cvt_pk_bf16_f32 v220, v46, v47
	v_cvt_pk_bf16_f32 v221, v48, v49
	v_cvt_pk_bf16_f32 v222, v42, v43
	v_cvt_pk_bf16_f32 v223, v44, v45
; __device__ __forceinline__ unsigned pk2(float lo, float hi) { const f32x2 v = {lo, hi}; const bf16x2_t b = __builtin_convertvector(v, bf16x2_t); return __builtin_bit_cast(unsigned, b); }
; __device__ __forceinline__ float sigm(float x) { return __builtin_amdgcn_rcpf(1.f + __expf(-x)); }
;     __device__ __forceinline__ void operator()(const f32x4 (&acc)[2][2][4][2], const Unit& u, int wr, int wc, int fr, int fq) const {
;         const int row0 = u.pm * BM + wr * 64 + fr, col0 = u.pn * BM + wc * 32 + 8 * fq;
; #pragma unroll
;         for (int ai = 0; ai < 2; ++ai)
; #pragma unroll
;             for (int m = 0; m < 4; ++m) { const size_t r = (size_t)(row0 + ai * HALF + m * 16);
; #pragma unroll
;                 for (int bj = 0; bj < 2; ++bj) { const int c = col0 + bj * HALF;
;                     const v4u pg = *(const v4u*)(P + r * NINP + GTO + c); const f32x4 b0 = *(const f32x4*)(bg + c), b1 = *(const f32x4*)(bg + c + 4);
;                     f32x4 g0, g1;
;                     g0[0] = sigm(__uint_as_float(pg.x << 16) + b0[0]); g0[1] = sigm(__uint_as_float(pg.x & 0xffff0000u) + b0[1]);
;                     g0[2] = sigm(__uint_as_float(pg.y << 16) + b0[2]); g0[3] = sigm(__uint_as_float(pg.y & 0xffff0000u) + b0[3]);
;                     g1[0] = sigm(__uint_as_float(pg.z << 16) + b1[0]); g1[1] = sigm(__uint_as_float(pg.z & 0xffff0000u) + b1[1]);
;                     g1[2] = sigm(__uint_as_float(pg.w << 16) + b1[2]); g1[3] = sigm(__uint_as_float(pg.w & 0xffff0000u) + b1[3]);
;                     const f32x4 t0 = g0 * acc[ai][bj][m][0], t1 = g1 * acc[ai][bj][m][1]; v4u tw; tw.x = pk2(t0[0], t0[1]); tw.y = pk2(t0[2], t0[3]); tw.z = pk2(t1[0], t1[1]); tw.w = pk2(t1[2], t1[3]);
;                     *(v4u*)(TMP + r * D + c) = tw; } }
;     }
	global_store_dwordx4 v[154:155], v[220:223], off
	v_lshlrev_b32_e32 v228, 16, v98
	v_and_b32_e32 v229, 0xffff0000, v98
	v_lshlrev_b32_e32 v230, 16, v99
	v_and_b32_e32 v231, 0xffff0000, v99
	v_lshlrev_b32_e32 v232, 16, v100
	v_and_b32_e32 v233, 0xffff0000, v100
	v_lshlrev_b32_e32 v234, 16, v101
	v_and_b32_e32 v235, 0xffff0000, v101
	v_add_f32_e32 v228, v212, v228
	v_add_f32_e32 v229, v213, v229
	v_add_f32_e32 v230, v214, v230
	v_add_f32_e32 v231, v215, v231
	v_add_f32_e32 v232, v216, v232
	v_add_f32_e32 v233, v217, v233
	v_add_f32_e32 v234, v218, v234
	v_add_f32_e32 v235, v219, v235
	v_mul_f32_e32 v228, 0xbfb8aa3b, v228
	v_mul_f32_e32 v229, 0xbfb8aa3b, v229
	v_mul_f32_e32 v230, 0xbfb8aa3b, v230
	v_mul_f32_e32 v231, 0xbfb8aa3b, v231
	v_mul_f32_e32 v232, 0xbfb8aa3b, v232
	v_mul_f32_e32 v233, 0xbfb8aa3b, v233
	v_mul_f32_e32 v234, 0xbfb8aa3b, v234
	v_mul_f32_e32 v235, 0xbfb8aa3b, v235
	v_exp_f32_e32 v228, v228
	v_exp_f32_e32 v229, v229
	v_exp_f32_e32 v230, v230
	v_exp_f32_e32 v231, v231
	v_exp_f32_e32 v232, v232
	v_exp_f32_e32 v233, v233
	v_exp_f32_e32 v234, v234
	v_exp_f32_e32 v235, v235
	v_add_f32_e32 v228, 1.0, v228
	v_add_f32_e32 v229, 1.0, v229
	v_add_f32_e32 v230, 1.0, v230
	v_add_f32_e32 v231, 1.0, v231
	v_add_f32_e32 v232, 1.0, v232
	v_add_f32_e32 v233, 1.0, v233
	v_add_f32_e32 v234, 1.0, v234
	v_add_f32_e32 v235, 1.0, v235
	v_rcp_f32_e32 v228, v228
	v_rcp_f32_e32 v229, v229
	v_rcp_f32_e32 v230, v230
	v_rcp_f32_e32 v231, v231
	v_rcp_f32_e32 v232, v232
	v_rcp_f32_e32 v233, v233
	v_rcp_f32_e32 v234, v234
	v_rcp_f32_e32 v235, v235
	v_pk_mul_f32 v[38:39], v[38:39], v[228:229]
	v_pk_mul_f32 v[40:41], v[40:41], v[230:231]
	v_pk_mul_f32 v[34:35], v[34:35], v[232:233]
	v_pk_mul_f32 v[36:37], v[36:37], v[234:235]
	v_cvt_pk_bf16_f32 v228, v38, v39
	v_cvt_pk_bf16_f32 v229, v40, v41
	v_cvt_pk_bf16_f32 v230, v34, v35
	v_cvt_pk_bf16_f32 v231, v36, v37
	global_store_dwordx4 v[154:155], v[228:231], off offset:256
	v_lshl_add_u64 v[154:155], v[154:155], 0, s[100:101]
	v_lshlrev_b32_e32 v220, 16, v90
	v_and_b32_e32 v221, 0xffff0000, v90
	v_lshlrev_b32_e32 v222, 16, v91
	v_and_b32_e32 v223, 0xffff0000, v91
	v_lshlrev_b32_e32 v224, 16, v92
	v_and_b32_e32 v225, 0xffff0000, v92
	v_lshlrev_b32_e32 v226, 16, v93
	v_and_b32_e32 v227, 0xffff0000, v93
	v_add_f32_e32 v220, v204, v220
	v_add_f32_e32 v221, v205, v221
	v_add_f32_e32 v222, v206, v222
	v_add_f32_e32 v223, v207, v223
	v_add_f32_e32 v224, v208, v224
	v_add_f32_e32 v225, v209, v225
	v_add_f32_e32 v226, v210, v226
	v_add_f32_e32 v227, v211, v227
	v_mul_f32_e32 v220, 0xbfb8aa3b, v220
	v_mul_f32_e32 v221, 0xbfb8aa3b, v221
	v_mul_f32_e32 v222, 0xbfb8aa3b, v222
	v_mul_f32_e32 v223, 0xbfb8aa3b, v223
	v_mul_f32_e32 v224, 0xbfb8aa3b, v224
	v_mul_f32_e32 v225, 0xbfb8aa3b, v225
	v_mul_f32_e32 v226, 0xbfb8aa3b, v226
	v_mul_f32_e32 v227, 0xbfb8aa3b, v227
	v_exp_f32_e32 v220, v220
	v_exp_f32_e32 v221, v221
	v_exp_f32_e32 v222, v222
	v_exp_f32_e32 v223, v223
	v_exp_f32_e32 v224, v224
	v_exp_f32_e32 v225, v225
	v_exp_f32_e32 v226, v226
	v_exp_f32_e32 v227, v227
	v_add_f32_e32 v220, 1.0, v220
	v_add_f32_e32 v221, 1.0, v221
	v_add_f32_e32 v222, 1.0, v222
	v_add_f32_e32 v223, 1.0, v223
	v_add_f32_e32 v224, 1.0, v224
	v_add_f32_e32 v225, 1.0, v225
	v_add_f32_e32 v226, 1.0, v226
	v_add_f32_e32 v227, 1.0, v227
	v_rcp_f32_e32 v220, v220
	v_rcp_f32_e32 v221, v221
	v_rcp_f32_e32 v222, v222
	v_rcp_f32_e32 v223, v223
	v_rcp_f32_e32 v224, v224
	v_rcp_f32_e32 v225, v225
	v_rcp_f32_e32 v226, v226
	v_rcp_f32_e32 v227, v227
	v_pk_mul_f32 v[30:31], v[30:31], v[220:221]
	v_pk_mul_f32 v[32:33], v[32:33], v[222:223]
	v_pk_mul_f32 v[26:27], v[26:27], v[224:225]
	v_pk_mul_f32 v[28:29], v[28:29], v[226:227]
	v_cvt_pk_bf16_f32 v220, v30, v31
	v_cvt_pk_bf16_f32 v221, v32, v33
	v_cvt_pk_bf16_f32 v222, v26, v27
	v_cvt_pk_bf16_f32 v223, v28, v29
	global_store_dwordx4 v[154:155], v[220:223], off
	v_lshlrev_b32_e32 v228, 16, v82
	v_and_b32_e32 v229, 0xffff0000, v82
	v_lshlrev_b32_e32 v230, 16, v83
	v_and_b32_e32 v231, 0xffff0000, v83
	v_lshlrev_b32_e32 v232, 16, v84
	v_and_b32_e32 v233, 0xffff0000, v84
	v_lshlrev_b32_e32 v234, 16, v85
	v_and_b32_e32 v235, 0xffff0000, v85
	v_add_f32_e32 v228, v212, v228
	v_add_f32_e32 v229, v213, v229
	v_add_f32_e32 v230, v214, v230
	v_add_f32_e32 v231, v215, v231
	v_add_f32_e32 v232, v216, v232
	v_add_f32_e32 v233, v217, v233
	v_add_f32_e32 v234, v218, v234
	v_add_f32_e32 v235, v219, v235
	v_mul_f32_e32 v228, 0xbfb8aa3b, v228
	v_mul_f32_e32 v229, 0xbfb8aa3b, v229
	v_mul_f32_e32 v230, 0xbfb8aa3b, v230
	v_mul_f32_e32 v231, 0xbfb8aa3b, v231
	v_mul_f32_e32 v232, 0xbfb8aa3b, v232
	v_mul_f32_e32 v233, 0xbfb8aa3b, v233
	v_mul_f32_e32 v234, 0xbfb8aa3b, v234
	v_mul_f32_e32 v235, 0xbfb8aa3b, v235
	v_exp_f32_e32 v228, v228
	v_exp_f32_e32 v229, v229
	v_exp_f32_e32 v230, v230
	v_exp_f32_e32 v231, v231
	v_exp_f32_e32 v232, v232
; __device__ __forceinline__ unsigned pk2(float lo, float hi) { const f32x2 v = {lo, hi}; const bf16x2_t b = __builtin_convertvector(v, bf16x2_t); return __builtin_bit_cast(unsigned, b); }
; __device__ __forceinline__ float sigm(float x) { return __builtin_amdgcn_rcpf(1.f + __expf(-x)); }
;     __device__ __forceinline__ void operator()(const f32x4 (&acc)[2][2][4][2], const Unit& u, int wr, int wc, int fr, int fq) const {
;         const int row0 = u.pm * BM + wr * 64 + fr, col0 = u.pn * BM + wc * 32 + 8 * fq;
; #pragma unroll
;         for (int ai = 0; ai < 2; ++ai)
; #pragma unroll
;             for (int m = 0; m < 4; ++m) { const size_t r = (size_t)(row0 + ai * HALF + m * 16);
; #pragma unroll
;                 for (int bj = 0; bj < 2; ++bj) { const int c = col0 + bj * HALF;
;                     const v4u pg = *(const v4u*)(P + r * NINP + GTO + c); const f32x4 b0 = *(const f32x4*)(bg + c), b1 = *(const f32x4*)(bg + c + 4);
;                     f32x4 g0, g1;
;                     g0[0] = sigm(__uint_as_float(pg.x << 16) + b0[0]); g0[1] = sigm(__uint_as_float(pg.x & 0xffff0000u) + b0[1]);
;                     g0[2] = sigm(__uint_as_float(pg.y << 16) + b0[2]); g0[3] = sigm(__uint_as_float(pg.y & 0xffff0000u) + b0[3]);
;                     g1[0] = sigm(__uint_as_float(pg.z << 16) + b1[0]); g1[1] = sigm(__uint_as_float(pg.z & 0xffff0000u) + b1[1]);
;                     g1[2] = sigm(__uint_as_float(pg.w << 16) + b1[2]); g1[3] = sigm(__uint_as_float(pg.w & 0xffff0000u) + b1[3]);
;                     const f32x4 t0 = g0 * acc[ai][bj][m][0], t1 = g1 * acc[ai][bj][m][1]; v4u tw; tw.x = pk2(t0[0], t0[1]); tw.y = pk2(t0[2], t0[3]); tw.z = pk2(t1[0], t1[1]); tw.w = pk2(t1[2], t1[3]);
;                     *(v4u*)(TMP + r * D + c) = tw; } }
;     }
	v_exp_f32_e32 v233, v233
	v_exp_f32_e32 v234, v234
	v_exp_f32_e32 v235, v235
	v_add_f32_e32 v228, 1.0, v228
	v_add_f32_e32 v229, 1.0, v229
	v_add_f32_e32 v230, 1.0, v230
	v_add_f32_e32 v231, 1.0, v231
	v_add_f32_e32 v232, 1.0, v232
	v_add_f32_e32 v233, 1.0, v233
	v_add_f32_e32 v234, 1.0, v234
	v_add_f32_e32 v235, 1.0, v235
	v_rcp_f32_e32 v228, v228
	v_rcp_f32_e32 v229, v229
	v_rcp_f32_e32 v230, v230
	v_rcp_f32_e32 v231, v231
	v_rcp_f32_e32 v232, v232
	v_rcp_f32_e32 v233, v233
	v_rcp_f32_e32 v234, v234
	v_rcp_f32_e32 v235, v235
	v_pk_mul_f32 v[22:23], v[22:23], v[228:229]
	v_pk_mul_f32 v[24:25], v[24:25], v[230:231]
	v_pk_mul_f32 v[18:19], v[18:19], v[232:233]
	v_pk_mul_f32 v[20:21], v[20:21], v[234:235]
	v_cvt_pk_bf16_f32 v228, v22, v23
	v_cvt_pk_bf16_f32 v229, v24, v25
	v_cvt_pk_bf16_f32 v230, v18, v19
	v_cvt_pk_bf16_f32 v231, v20, v21
	global_store_dwordx4 v[154:155], v[228:231], off offset:256
	v_lshl_add_u64 v[154:155], v[154:155], 0, s[100:101]
	v_lshlrev_b32_e32 v220, 16, v74
	v_and_b32_e32 v221, 0xffff0000, v74
	v_lshlrev_b32_e32 v222, 16, v75
	v_and_b32_e32 v223, 0xffff0000, v75
	v_lshlrev_b32_e32 v224, 16, v76
	v_and_b32_e32 v225, 0xffff0000, v76
	v_lshlrev_b32_e32 v226, 16, v77
	v_and_b32_e32 v227, 0xffff0000, v77
	v_add_f32_e32 v220, v204, v220
	v_add_f32_e32 v221, v205, v221
	v_add_f32_e32 v222, v206, v222
	v_add_f32_e32 v223, v207, v223
	v_add_f32_e32 v224, v208, v224
	v_add_f32_e32 v225, v209, v225
	v_add_f32_e32 v226, v210, v226
	v_add_f32_e32 v227, v211, v227
	v_mul_f32_e32 v220, 0xbfb8aa3b, v220
	v_mul_f32_e32 v221, 0xbfb8aa3b, v221
	v_mul_f32_e32 v222, 0xbfb8aa3b, v222
	v_mul_f32_e32 v223, 0xbfb8aa3b, v223
	v_mul_f32_e32 v224, 0xbfb8aa3b, v224
	v_mul_f32_e32 v225, 0xbfb8aa3b, v225
	v_mul_f32_e32 v226, 0xbfb8aa3b, v226
	v_mul_f32_e32 v227, 0xbfb8aa3b, v227
	v_exp_f32_e32 v220, v220
	v_exp_f32_e32 v221, v221
	v_exp_f32_e32 v222, v222
	v_exp_f32_e32 v223, v223
	v_exp_f32_e32 v224, v224
	v_exp_f32_e32 v225, v225
	v_exp_f32_e32 v226, v226
	v_exp_f32_e32 v227, v227
	v_add_f32_e32 v220, 1.0, v220
	v_add_f32_e32 v221, 1.0, v221
	v_add_f32_e32 v222, 1.0, v222
	v_add_f32_e32 v223, 1.0, v223
	v_add_f32_e32 v224, 1.0, v224
	v_add_f32_e32 v225, 1.0, v225
	v_add_f32_e32 v226, 1.0, v226
	v_add_f32_e32 v227, 1.0, v227
	v_rcp_f32_e32 v220, v220
	v_rcp_f32_e32 v221, v221
	v_rcp_f32_e32 v222, v222
	v_rcp_f32_e32 v223, v223
	v_rcp_f32_e32 v224, v224
	v_rcp_f32_e32 v225, v225
	v_rcp_f32_e32 v226, v226
	v_rcp_f32_e32 v227, v227
	v_pk_mul_f32 v[14:15], v[14:15], v[220:221]
	v_pk_mul_f32 v[16:17], v[16:17], v[222:223]
	v_pk_mul_f32 v[10:11], v[10:11], v[224:225]
	v_pk_mul_f32 v[12:13], v[12:13], v[226:227]
	v_cvt_pk_bf16_f32 v220, v14, v15
	v_cvt_pk_bf16_f32 v221, v16, v17
	v_cvt_pk_bf16_f32 v222, v10, v11
	v_cvt_pk_bf16_f32 v223, v12, v13
	global_store_dwordx4 v[154:155], v[220:223], off
	v_lshlrev_b32_e32 v228, 16, v66
	v_and_b32_e32 v229, 0xffff0000, v66
	v_lshlrev_b32_e32 v230, 16, v67
	v_and_b32_e32 v231, 0xffff0000, v67
	v_lshlrev_b32_e32 v232, 16, v68
	v_and_b32_e32 v233, 0xffff0000, v68
	v_lshlrev_b32_e32 v234, 16, v69
	v_and_b32_e32 v235, 0xffff0000, v69
	v_add_f32_e32 v228, v212, v228
	v_add_f32_e32 v229, v213, v229
	v_add_f32_e32 v230, v214, v230
	v_add_f32_e32 v231, v215, v231
	v_add_f32_e32 v232, v216, v232
	v_add_f32_e32 v233, v217, v233
	v_add_f32_e32 v234, v218, v234
	v_add_f32_e32 v235, v219, v235
	v_mul_f32_e32 v228, 0xbfb8aa3b, v228
	v_mul_f32_e32 v229, 0xbfb8aa3b, v229
	v_mul_f32_e32 v230, 0xbfb8aa3b, v230
	v_mul_f32_e32 v231, 0xbfb8aa3b, v231
	v_mul_f32_e32 v232, 0xbfb8aa3b, v232
	v_mul_f32_e32 v233, 0xbfb8aa3b, v233
	v_mul_f32_e32 v234, 0xbfb8aa3b, v234
	v_mul_f32_e32 v235, 0xbfb8aa3b, v235
	v_exp_f32_e32 v228, v228
	v_exp_f32_e32 v229, v229
	v_exp_f32_e32 v230, v230
	v_exp_f32_e32 v231, v231
	v_exp_f32_e32 v232, v232
	v_exp_f32_e32 v233, v233
	v_exp_f32_e32 v234, v234
	v_exp_f32_e32 v235, v235
	v_add_f32_e32 v228, 1.0, v228
	v_add_f32_e32 v229, 1.0, v229
	v_add_f32_e32 v230, 1.0, v230
	v_add_f32_e32 v231, 1.0, v231
	v_add_f32_e32 v232, 1.0, v232
	v_add_f32_e32 v233, 1.0, v233
	v_add_f32_e32 v234, 1.0, v234
	v_add_f32_e32 v235, 1.0, v235
	v_rcp_f32_e32 v228, v228
	v_rcp_f32_e32 v229, v229
	v_rcp_f32_e32 v230, v230
	v_rcp_f32_e32 v231, v231
	v_rcp_f32_e32 v232, v232
	v_rcp_f32_e32 v233, v233
	v_rcp_f32_e32 v234, v234
	v_rcp_f32_e32 v235, v235
	v_pk_mul_f32 v[6:7], v[6:7], v[228:229]
	v_pk_mul_f32 v[8:9], v[8:9], v[230:231]
	v_pk_mul_f32 v[2:3], v[2:3], v[232:233]
	v_pk_mul_f32 v[4:5], v[4:5], v[234:235]
	v_cvt_pk_bf16_f32 v228, v6, v7
	v_cvt_pk_bf16_f32 v229, v8, v9
	v_cvt_pk_bf16_f32 v230, v2, v3
	v_cvt_pk_bf16_f32 v231, v4, v5
	global_store_dwordx4 v[154:155], v[228:231], off offset:256
	s_mov_b64 s[2:3], -1
	s_cbranch_vccnz .LBB0_1250
	s_andn2_b64 vcc, exec, s[12:13]
	s_cbranch_vccnz .LBB0_1249
	s_barrier
	s_branch .LBB0_1249

; __device__ __forceinline__ unsigned cvt_pk_bf16(float lo, float hi) { unsigned r; asm volatile("v_cvt_pk_bf16_f32 %0, %1, %2" : "=v"(r) : "v"(lo), "v"(hi)); return r; }
; __device__ __forceinline__ float sigm(float x) { return __builtin_amdgcn_rcpf(1.f + __expf(-x)); }
;     __device__ __forceinline__ void operator()(const f32x4 (&acc)[2][2][4][2], const Unit& u, int wr, int wc, int fr, int fq) const {
;         const int row0 = u.pm * BM + wr * 64 + fr, col0 = u.pn * BM + wc * 32 + 8 * fq;
; #pragma unroll
;         for (int ai = 0; ai < 2; ++ai)
; #pragma unroll
;             for (int m = 0; m < 4; ++m) { const size_t r = (size_t)(row0 + ai * HALF + m * 16);
; #pragma unroll
;                 for (int bj = 0; bj < 2; ++bj) { const int c = col0 + bj * HALF;
;                     const v4u pg = *(const v4u*)(P + r * NINP + GTO + D + c); const f32x4 b0 = *(const f32x4*)(bg + D + c), b1 = *(const f32x4*)(bg + D + c + 4);
;                     const v4u tw = *(const v4u*)(TMP + r * D + c); const f32x4 t0 = (f32x4){__uint_as_float(tw.x << 16), __uint_as_float(tw.x & 0xffff0000u), __uint_as_float(tw.y << 16), __uint_as_float(tw.y & 0xffff0000u)}, t1 = (f32x4){__uint_as_float(tw.z << 16), __uint_as_float(tw.z & 0xffff0000u), __uint_as_float(tw.w << 16), __uint_as_float(tw.w & 0xffff0000u)};
;                     f32x4 g0, g1;
;                     g0[0] = sigm(__uint_as_float(pg.x << 16) + b0[0]); g0[1] = sigm(__uint_as_float(pg.x & 0xffff0000u) + b0[1]);
;                     g0[2] = sigm(__uint_as_float(pg.y << 16) + b0[2]); g0[3] = sigm(__uint_as_float(pg.y & 0xffff0000u) + b0[3]);
;                     g1[0] = sigm(__uint_as_float(pg.z << 16) + b1[0]); g1[1] = sigm(__uint_as_float(pg.z & 0xffff0000u) + b1[1]);
;                     g1[2] = sigm(__uint_as_float(pg.w << 16) + b1[2]); g1[3] = sigm(__uint_as_float(pg.w & 0xffff0000u) + b1[3]);
;                     const f32x4 v0 = t0 + g0 * acc[ai][bj][m][0], v1 = t1 + g1 * acc[ai][bj][m][1];
;                     v4u w; w.x = pg8::cvt_pk_bf16(v0[0], v0[1]); w.y = pg8::cvt_pk_bf16(v0[2], v0[3]); w.z = pg8::cvt_pk_bf16(v1[0], v1[1]); w.w = pg8::cvt_pk_bf16(v1[2], v1[3]);
;                     *(v4u*)(MRG + r * D + c) = w; } }
;     }
.LBB0_1285:
	v_lshl_add_u32 v152, s2, 8, v154
	v_lshl_or_b32 v160, s3, 8, v159
	v_mov_b64_e32 v[148:149], s[10:11]
	v_mad_i64_i32 v[146:147], s[2:3], v152, s54, v[148:149]
	v_ashrrev_i32_e32 v161, 31, v160
	v_lshl_add_u64 v[146:147], v[146:147], 0, s[20:21]
	v_lshlrev_b64 v[148:149], 1, v[160:161]
	v_ashrrev_i32_e32 v153, 31, v152
	v_lshl_add_u64 v[146:147], v[146:147], 0, v[148:149]
	v_lshlrev_b64 v[150:151], 12, v[152:153]
	v_lshl_add_u64 v[238:239], s[8:9], 0, v[150:151]
	v_lshl_add_u64 v[238:239], v[238:239], 0, v[148:149]
	v_lshl_add_u64 v[240:241], s[12:13], 0, v[150:151]
	v_lshl_add_u64 v[240:241], v[240:241], 0, v[148:149]
	v_lshl_add_u64 v[242:243], v[160:161], 2, s[18:19]
	s_andn2_b64 vcc, exec, s[4:5]
	s_lshl_b32 s98, s54, 4
	s_mov_b32 s99, 0
	s_mov_b32 s100, 0x10000
	s_mov_b32 s101, 0
	global_load_dwordx4 v[196:199], v[242:243], off
	global_load_dwordx4 v[200:203], v[242:243], off offset:16
	global_load_dwordx4 v[204:207], v[242:243], off offset:512
	global_load_dwordx4 v[208:211], v[242:243], off offset:528
	v_lshl_add_u64 v[244:245], s[98:99], 3, v[146:147]
	v_lshl_add_u64 v[246:247], s[100:101], 3, v[238:239]
	v_lshl_add_u64 v[150:151], s[100:101], 3, v[240:241]
	global_load_dwordx4 v[164:167], v[146:147], off
	global_load_dwordx4 v[168:171], v[238:239], off
	global_load_dwordx4 v[172:175], v[146:147], off offset:256
	global_load_dwordx4 v[176:179], v[238:239], off offset:256
	v_lshl_add_u64 v[146:147], v[146:147], 0, s[98:99]
	v_lshl_add_u64 v[238:239], v[238:239], 0, s[100:101]
	global_load_dwordx4 v[180:183], v[146:147], off
	global_load_dwordx4 v[184:187], v[238:239], off
	global_load_dwordx4 v[188:191], v[146:147], off offset:256
	global_load_dwordx4 v[192:195], v[238:239], off offset:256
	s_waitcnt vmcnt(0)
	v_lshlrev_b32_e32 v212, 16, v164
	v_and_b32_e32 v213, 0xffff0000, v164
	v_lshlrev_b32_e32 v214, 16, v165
	v_and_b32_e32 v215, 0xffff0000, v165
	v_lshlrev_b32_e32 v216, 16, v166
	v_and_b32_e32 v217, 0xffff0000, v166
	v_lshlrev_b32_e32 v218, 16, v167
	v_and_b32_e32 v219, 0xffff0000, v167
	v_add_f32_e32 v212, v196, v212
	v_add_f32_e32 v213, v197, v213
	v_add_f32_e32 v214, v198, v214
	v_add_f32_e32 v215, v199, v215
	v_add_f32_e32 v216, v200, v216
	v_add_f32_e32 v217, v201, v217
	v_add_f32_e32 v218, v202, v218
	v_add_f32_e32 v219, v203, v219
	v_mul_f32_e32 v212, 0xbfb8aa3b, v212
	v_mul_f32_e32 v213, 0xbfb8aa3b, v213
	v_mul_f32_e32 v214, 0xbfb8aa3b, v214
	v_mul_f32_e32 v215, 0xbfb8aa3b, v215
	v_mul_f32_e32 v216, 0xbfb8aa3b, v216
	v_mul_f32_e32 v217, 0xbfb8aa3b, v217
	v_mul_f32_e32 v218, 0xbfb8aa3b, v218
	v_mul_f32_e32 v219, 0xbfb8aa3b, v219
	v_exp_f32_e32 v212, v212
	v_exp_f32_e32 v213, v213
	v_exp_f32_e32 v214, v214
	v_exp_f32_e32 v215, v215
	v_exp_f32_e32 v216, v216
	v_exp_f32_e32 v217, v217
	v_exp_f32_e32 v218, v218
	v_exp_f32_e32 v219, v219
	v_add_f32_e32 v212, 1.0, v212
	v_add_f32_e32 v213, 1.0, v213
	v_add_f32_e32 v214, 1.0, v214
	v_add_f32_e32 v215, 1.0, v215
	v_add_f32_e32 v216, 1.0, v216
	v_add_f32_e32 v217, 1.0, v217
	v_add_f32_e32 v218, 1.0, v218
	v_add_f32_e32 v219, 1.0, v219
	v_rcp_f32_e32 v212, v212
	v_rcp_f32_e32 v213, v213
	v_rcp_f32_e32 v214, v214
	v_rcp_f32_e32 v215, v215
	v_rcp_f32_e32 v216, v216
	v_rcp_f32_e32 v217, v217
	v_rcp_f32_e32 v218, v218
	v_rcp_f32_e32 v219, v219
	v_lshlrev_b32_e32 v164, 16, v168
	v_and_b32_e32 v165, 0xffff0000, v168
	v_lshlrev_b32_e32 v166, 16, v169
	v_and_b32_e32 v167, 0xffff0000, v169
	v_pk_fma_f32 v[126:127], v[126:127], v[212:213], v[164:165]
	v_pk_fma_f32 v[128:129], v[128:129], v[214:215], v[166:167]
	v_lshlrev_b32_e32 v168, 16, v170
	v_and_b32_e32 v169, 0xffff0000, v170
	v_lshlrev_b32_e32 v170, 16, v171
	v_and_b32_e32 v171, 0xffff0000, v171
	v_pk_fma_f32 v[122:123], v[122:123], v[216:217], v[168:169]
	v_pk_fma_f32 v[124:125], v[124:125], v[218:219], v[170:171]
	v_cvt_pk_bf16_f32 v212, v126, v127
	v_cvt_pk_bf16_f32 v213, v128, v129
	v_cvt_pk_bf16_f32 v214, v122, v123
	v_cvt_pk_bf16_f32 v215, v124, v125
	global_store_dwordx4 v[240:241], v[212:215], off
	v_lshlrev_b32_e32 v220, 16, v172
	v_and_b32_e32 v221, 0xffff0000, v172
	v_lshlrev_b32_e32 v222, 16, v173
	v_and_b32_e32 v223, 0xffff0000, v173
	v_lshlrev_b32_e32 v224, 16, v174
	v_and_b32_e32 v225, 0xffff0000, v174
	v_lshlrev_b32_e32 v226, 16, v175
	v_and_b32_e32 v227, 0xffff0000, v175
	v_add_f32_e32 v220, v204, v220
	v_add_f32_e32 v221, v205, v221
	v_add_f32_e32 v222, v206, v222
	v_add_f32_e32 v223, v207, v223
	v_add_f32_e32 v224, v208, v224
	v_add_f32_e32 v225, v209, v225
	v_add_f32_e32 v226, v210, v226
	v_add_f32_e32 v227, v211, v227
	v_mul_f32_e32 v220, 0xbfb8aa3b, v220
	v_mul_f32_e32 v221, 0xbfb8aa3b, v221
	v_mul_f32_e32 v222, 0xbfb8aa3b, v222
	v_mul_f32_e32 v223, 0xbfb8aa3b, v223
	v_mul_f32_e32 v224, 0xbfb8aa3b, v224
	v_mul_f32_e32 v225, 0xbfb8aa3b, v225
	v_mul_f32_e32 v226, 0xbfb8aa3b, v226
	v_mul_f32_e32 v227, 0xbfb8aa3b, v227
	v_exp_f32_e32 v220, v220
	v_exp_f32_e32 v221, v221
	v_exp_f32_e32 v222, v222
	v_exp_f32_e32 v223, v223
	v_exp_f32_e32 v224, v224
	v_exp_f32_e32 v225, v225
	v_exp_f32_e32 v226, v226
	v_exp_f32_e32 v227, v227
	v_add_f32_e32 v220, 1.0, v220
	v_add_f32_e32 v221, 1.0, v221
	v_add_f32_e32 v222, 1.0, v222
	v_add_f32_e32 v223, 1.0, v223
	v_add_f32_e32 v224, 1.0, v224
	v_add_f32_e32 v225, 1.0, v225
	v_add_f32_e32 v226, 1.0, v226
	v_add_f32_e32 v227, 1.0, v227
	v_rcp_f32_e32 v220, v220
	v_rcp_f32_e32 v221, v221
	v_rcp_f32_e32 v222, v222
	v_rcp_f32_e32 v223, v223
	v_rcp_f32_e32 v224, v224
	v_rcp_f32_e32 v225, v225
	v_rcp_f32_e32 v226, v226
	v_rcp_f32_e32 v227, v227
	v_lshlrev_b32_e32 v172, 16, v176
	v_and_b32_e32 v173, 0xffff0000, v176
	v_lshlrev_b32_e32 v174, 16, v177
	v_and_b32_e32 v175, 0xffff0000, v177
; __device__ __forceinline__ unsigned cvt_pk_bf16(float lo, float hi) { unsigned r; asm volatile("v_cvt_pk_bf16_f32 %0, %1, %2" : "=v"(r) : "v"(lo), "v"(hi)); return r; }
; __device__ __forceinline__ float sigm(float x) { return __builtin_amdgcn_rcpf(1.f + __expf(-x)); }
;     __device__ __forceinline__ void operator()(const f32x4 (&acc)[2][2][4][2], const Unit& u, int wr, int wc, int fr, int fq) const {
;         const int row0 = u.pm * BM + wr * 64 + fr, col0 = u.pn * BM + wc * 32 + 8 * fq;
; #pragma unroll
;         for (int ai = 0; ai < 2; ++ai)
; #pragma unroll
;             for (int m = 0; m < 4; ++m) { const size_t r = (size_t)(row0 + ai * HALF + m * 16);
; #pragma unroll
;                 for (int bj = 0; bj < 2; ++bj) { const int c = col0 + bj * HALF;
;                     const v4u pg = *(const v4u*)(P + r * NINP + GTO + D + c); const f32x4 b0 = *(const f32x4*)(bg + D + c), b1 = *(const f32x4*)(bg + D + c + 4);
;                     const v4u tw = *(const v4u*)(TMP + r * D + c); const f32x4 t0 = (f32x4){__uint_as_float(tw.x << 16), __uint_as_float(tw.x & 0xffff0000u), __uint_as_float(tw.y << 16), __uint_as_float(tw.y & 0xffff0000u)}, t1 = (f32x4){__uint_as_float(tw.z << 16), __uint_as_float(tw.z & 0xffff0000u), __uint_as_float(tw.w << 16), __uint_as_float(tw.w & 0xffff0000u)};
;                     f32x4 g0, g1;
;                     g0[0] = sigm(__uint_as_float(pg.x << 16) + b0[0]); g0[1] = sigm(__uint_as_float(pg.x & 0xffff0000u) + b0[1]);
;                     g0[2] = sigm(__uint_as_float(pg.y << 16) + b0[2]); g0[3] = sigm(__uint_as_float(pg.y & 0xffff0000u) + b0[3]);
;                     g1[0] = sigm(__uint_as_float(pg.z << 16) + b1[0]); g1[1] = sigm(__uint_as_float(pg.z & 0xffff0000u) + b1[1]);
;                     g1[2] = sigm(__uint_as_float(pg.w << 16) + b1[2]); g1[3] = sigm(__uint_as_float(pg.w & 0xffff0000u) + b1[3]);
;                     const f32x4 v0 = t0 + g0 * acc[ai][bj][m][0], v1 = t1 + g1 * acc[ai][bj][m][1];
;                     v4u w; w.x = pg8::cvt_pk_bf16(v0[0], v0[1]); w.y = pg8::cvt_pk_bf16(v0[2], v0[3]); w.z = pg8::cvt_pk_bf16(v1[0], v1[1]); w.w = pg8::cvt_pk_bf16(v1[2], v1[3]);
;                     *(v4u*)(MRG + r * D + c) = w; } }
;     }
	v_pk_fma_f32 v[118:119], v[118:119], v[220:221], v[172:173]
	v_pk_fma_f32 v[120:121], v[120:121], v[222:223], v[174:175]
	v_lshlrev_b32_e32 v176, 16, v178
	v_and_b32_e32 v177, 0xffff0000, v178
	v_lshlrev_b32_e32 v178, 16, v179
	v_and_b32_e32 v179, 0xffff0000, v179
	v_pk_fma_f32 v[114:115], v[114:115], v[224:225], v[176:177]
	v_pk_fma_f32 v[116:117], v[116:117], v[226:227], v[178:179]
	v_cvt_pk_bf16_f32 v220, v118, v119
	v_cvt_pk_bf16_f32 v221, v120, v121
	v_cvt_pk_bf16_f32 v222, v114, v115
	v_cvt_pk_bf16_f32 v223, v116, v117
	global_store_dwordx4 v[240:241], v[220:223], off offset:256
	v_lshl_add_u64 v[240:241], v[240:241], 0, s[100:101]
	v_lshlrev_b32_e32 v212, 16, v180
	v_and_b32_e32 v213, 0xffff0000, v180
	v_lshlrev_b32_e32 v214, 16, v181
	v_and_b32_e32 v215, 0xffff0000, v181
	v_lshlrev_b32_e32 v216, 16, v182
	v_and_b32_e32 v217, 0xffff0000, v182
	v_lshlrev_b32_e32 v218, 16, v183
	v_and_b32_e32 v219, 0xffff0000, v183
	v_add_f32_e32 v212, v196, v212
	v_add_f32_e32 v213, v197, v213
	v_add_f32_e32 v214, v198, v214
	v_add_f32_e32 v215, v199, v215
	v_add_f32_e32 v216, v200, v216
	v_add_f32_e32 v217, v201, v217
	v_add_f32_e32 v218, v202, v218
	v_add_f32_e32 v219, v203, v219
	v_mul_f32_e32 v212, 0xbfb8aa3b, v212
	v_mul_f32_e32 v213, 0xbfb8aa3b, v213
	v_mul_f32_e32 v214, 0xbfb8aa3b, v214
	v_mul_f32_e32 v215, 0xbfb8aa3b, v215
	v_mul_f32_e32 v216, 0xbfb8aa3b, v216
	v_mul_f32_e32 v217, 0xbfb8aa3b, v217
	v_mul_f32_e32 v218, 0xbfb8aa3b, v218
	v_mul_f32_e32 v219, 0xbfb8aa3b, v219
	v_exp_f32_e32 v212, v212
	v_exp_f32_e32 v213, v213
	v_exp_f32_e32 v214, v214
	v_exp_f32_e32 v215, v215
	v_exp_f32_e32 v216, v216
	v_exp_f32_e32 v217, v217
	v_exp_f32_e32 v218, v218
	v_exp_f32_e32 v219, v219
	v_add_f32_e32 v212, 1.0, v212
	v_add_f32_e32 v213, 1.0, v213
	v_add_f32_e32 v214, 1.0, v214
	v_add_f32_e32 v215, 1.0, v215
	v_add_f32_e32 v216, 1.0, v216
	v_add_f32_e32 v217, 1.0, v217
	v_add_f32_e32 v218, 1.0, v218
	v_add_f32_e32 v219, 1.0, v219
	v_rcp_f32_e32 v212, v212
	v_rcp_f32_e32 v213, v213
	v_rcp_f32_e32 v214, v214
	v_rcp_f32_e32 v215, v215
	v_rcp_f32_e32 v216, v216
	v_rcp_f32_e32 v217, v217
	v_rcp_f32_e32 v218, v218
	v_rcp_f32_e32 v219, v219
	v_lshlrev_b32_e32 v180, 16, v184
	v_and_b32_e32 v181, 0xffff0000, v184
	v_lshlrev_b32_e32 v182, 16, v185
	v_and_b32_e32 v183, 0xffff0000, v185
	v_pk_fma_f32 v[110:111], v[110:111], v[212:213], v[180:181]
	v_pk_fma_f32 v[112:113], v[112:113], v[214:215], v[182:183]
	v_lshlrev_b32_e32 v184, 16, v186
	v_and_b32_e32 v185, 0xffff0000, v186
	v_lshlrev_b32_e32 v186, 16, v187
	v_and_b32_e32 v187, 0xffff0000, v187
	v_pk_fma_f32 v[106:107], v[106:107], v[216:217], v[184:185]
	v_pk_fma_f32 v[108:109], v[108:109], v[218:219], v[186:187]
	v_cvt_pk_bf16_f32 v212, v110, v111
	v_cvt_pk_bf16_f32 v213, v112, v113
	v_cvt_pk_bf16_f32 v214, v106, v107
	v_cvt_pk_bf16_f32 v215, v108, v109
	global_store_dwordx4 v[240:241], v[212:215], off
	v_lshlrev_b32_e32 v220, 16, v188
	v_and_b32_e32 v221, 0xffff0000, v188
	v_lshlrev_b32_e32 v222, 16, v189
	v_and_b32_e32 v223, 0xffff0000, v189
	v_lshlrev_b32_e32 v224, 16, v190
	v_and_b32_e32 v225, 0xffff0000, v190
	v_lshlrev_b32_e32 v226, 16, v191
	v_and_b32_e32 v227, 0xffff0000, v191
	v_add_f32_e32 v220, v204, v220
	v_add_f32_e32 v221, v205, v221
	v_add_f32_e32 v222, v206, v222
	v_add_f32_e32 v223, v207, v223
	v_add_f32_e32 v224, v208, v224
	v_add_f32_e32 v225, v209, v225
	v_add_f32_e32 v226, v210, v226
	v_add_f32_e32 v227, v211, v227
	v_mul_f32_e32 v220, 0xbfb8aa3b, v220
	v_mul_f32_e32 v221, 0xbfb8aa3b, v221
	v_mul_f32_e32 v222, 0xbfb8aa3b, v222
	v_mul_f32_e32 v223, 0xbfb8aa3b, v223
	v_mul_f32_e32 v224, 0xbfb8aa3b, v224
	v_mul_f32_e32 v225, 0xbfb8aa3b, v225
	v_mul_f32_e32 v226, 0xbfb8aa3b, v226
	v_mul_f32_e32 v227, 0xbfb8aa3b, v227
	v_exp_f32_e32 v220, v220
	v_exp_f32_e32 v221, v221
	v_exp_f32_e32 v222, v222
	v_exp_f32_e32 v223, v223
	v_exp_f32_e32 v224, v224
	v_exp_f32_e32 v225, v225
	v_exp_f32_e32 v226, v226
	v_exp_f32_e32 v227, v227
	v_add_f32_e32 v220, 1.0, v220
	v_add_f32_e32 v221, 1.0, v221
	v_add_f32_e32 v222, 1.0, v222
	v_add_f32_e32 v223, 1.0, v223
	v_add_f32_e32 v224, 1.0, v224
	v_add_f32_e32 v225, 1.0, v225
	v_add_f32_e32 v226, 1.0, v226
	v_add_f32_e32 v227, 1.0, v227
	v_rcp_f32_e32 v220, v220
	v_rcp_f32_e32 v221, v221
	v_rcp_f32_e32 v222, v222
	v_rcp_f32_e32 v223, v223
	v_rcp_f32_e32 v224, v224
	v_rcp_f32_e32 v225, v225
	v_rcp_f32_e32 v226, v226
	v_rcp_f32_e32 v227, v227
	v_lshlrev_b32_e32 v188, 16, v192
	v_and_b32_e32 v189, 0xffff0000, v192
	v_lshlrev_b32_e32 v190, 16, v193
	v_and_b32_e32 v191, 0xffff0000, v193
	v_pk_fma_f32 v[102:103], v[102:103], v[220:221], v[188:189]
	v_pk_fma_f32 v[104:105], v[104:105], v[222:223], v[190:191]
	v_lshlrev_b32_e32 v192, 16, v194
	v_and_b32_e32 v193, 0xffff0000, v194
	v_lshlrev_b32_e32 v194, 16, v195
	v_and_b32_e32 v195, 0xffff0000, v195
	v_pk_fma_f32 v[98:99], v[98:99], v[224:225], v[192:193]
	v_pk_fma_f32 v[100:101], v[100:101], v[226:227], v[194:195]
	v_cvt_pk_bf16_f32 v220, v102, v103
	v_cvt_pk_bf16_f32 v221, v104, v105
	v_cvt_pk_bf16_f32 v222, v98, v99
	v_cvt_pk_bf16_f32 v223, v100, v101
	global_store_dwordx4 v[240:241], v[220:223], off offset:256
	v_lshl_add_u64 v[146:147], v[146:147], 0, s[98:99]
	v_lshl_add_u64 v[238:239], v[238:239], 0, s[100:101]
	global_load_dwordx4 v[164:167], v[146:147], off
	global_load_dwordx4 v[168:171], v[238:239], off
	global_load_dwordx4 v[172:175], v[146:147], off offset:256
	global_load_dwordx4 v[176:179], v[238:239], off offset:256
	v_lshl_add_u64 v[146:147], v[146:147], 0, s[98:99]
	v_lshl_add_u64 v[238:239], v[238:239], 0, s[100:101]
	global_load_dwordx4 v[180:183], v[146:147], off
	global_load_dwordx4 v[184:187], v[238:239], off
	global_load_dwordx4 v[188:191], v[146:147], off offset:256
	global_load_dwordx4 v[192:195], v[238:239], off offset:256
	s_waitcnt vmcnt(0)
; __device__ __forceinline__ unsigned cvt_pk_bf16(float lo, float hi) { unsigned r; asm volatile("v_cvt_pk_bf16_f32 %0, %1, %2" : "=v"(r) : "v"(lo), "v"(hi)); return r; }
; __device__ __forceinline__ float sigm(float x) { return __builtin_amdgcn_rcpf(1.f + __expf(-x)); }
;     __device__ __forceinline__ void operator()(const f32x4 (&acc)[2][2][4][2], const Unit& u, int wr, int wc, int fr, int fq) const {
;         const int row0 = u.pm * BM + wr * 64 + fr, col0 = u.pn * BM + wc * 32 + 8 * fq;
; #pragma unroll
;         for (int ai = 0; ai < 2; ++ai)
; #pragma unroll
;             for (int m = 0; m < 4; ++m) { const size_t r = (size_t)(row0 + ai * HALF + m * 16);
; #pragma unroll
;                 for (int bj = 0; bj < 2; ++bj) { const int c = col0 + bj * HALF;
;                     const v4u pg = *(const v4u*)(P + r * NINP + GTO + D + c); const f32x4 b0 = *(const f32x4*)(bg + D + c), b1 = *(const f32x4*)(bg + D + c + 4);
;                     const v4u tw = *(const v4u*)(TMP + r * D + c); const f32x4 t0 = (f32x4){__uint_as_float(tw.x << 16), __uint_as_float(tw.x & 0xffff0000u), __uint_as_float(tw.y << 16), __uint_as_float(tw.y & 0xffff0000u)}, t1 = (f32x4){__uint_as_float(tw.z << 16), __uint_as_float(tw.z & 0xffff0000u), __uint_as_float(tw.w << 16), __uint_as_float(tw.w & 0xffff0000u)};
;                     f32x4 g0, g1;
;                     g0[0] = sigm(__uint_as_float(pg.x << 16) + b0[0]); g0[1] = sigm(__uint_as_float(pg.x & 0xffff0000u) + b0[1]);
;                     g0[2] = sigm(__uint_as_float(pg.y << 16) + b0[2]); g0[3] = sigm(__uint_as_float(pg.y & 0xffff0000u) + b0[3]);
;                     g1[0] = sigm(__uint_as_float(pg.z << 16) + b1[0]); g1[1] = sigm(__uint_as_float(pg.z & 0xffff0000u) + b1[1]);
;                     g1[2] = sigm(__uint_as_float(pg.w << 16) + b1[2]); g1[3] = sigm(__uint_as_float(pg.w & 0xffff0000u) + b1[3]);
;                     const f32x4 v0 = t0 + g0 * acc[ai][bj][m][0], v1 = t1 + g1 * acc[ai][bj][m][1];
;                     v4u w; w.x = pg8::cvt_pk_bf16(v0[0], v0[1]); w.y = pg8::cvt_pk_bf16(v0[2], v0[3]); w.z = pg8::cvt_pk_bf16(v1[0], v1[1]); w.w = pg8::cvt_pk_bf16(v1[2], v1[3]);
;                     *(v4u*)(MRG + r * D + c) = w; } }
;     }
	v_lshl_add_u64 v[240:241], v[240:241], 0, s[100:101]
	v_lshlrev_b32_e32 v212, 16, v164
	v_and_b32_e32 v213, 0xffff0000, v164
	v_lshlrev_b32_e32 v214, 16, v165
	v_and_b32_e32 v215, 0xffff0000, v165
	v_lshlrev_b32_e32 v216, 16, v166
	v_and_b32_e32 v217, 0xffff0000, v166
	v_lshlrev_b32_e32 v218, 16, v167
	v_and_b32_e32 v219, 0xffff0000, v167
	v_add_f32_e32 v212, v196, v212
	v_add_f32_e32 v213, v197, v213
	v_add_f32_e32 v214, v198, v214
	v_add_f32_e32 v215, v199, v215
	v_add_f32_e32 v216, v200, v216
	v_add_f32_e32 v217, v201, v217
	v_add_f32_e32 v218, v202, v218
	v_add_f32_e32 v219, v203, v219
	v_mul_f32_e32 v212, 0xbfb8aa3b, v212
	v_mul_f32_e32 v213, 0xbfb8aa3b, v213
	v_mul_f32_e32 v214, 0xbfb8aa3b, v214
	v_mul_f32_e32 v215, 0xbfb8aa3b, v215
	v_mul_f32_e32 v216, 0xbfb8aa3b, v216
	v_mul_f32_e32 v217, 0xbfb8aa3b, v217
	v_mul_f32_e32 v218, 0xbfb8aa3b, v218
	v_mul_f32_e32 v219, 0xbfb8aa3b, v219
	v_exp_f32_e32 v212, v212
	v_exp_f32_e32 v213, v213
	v_exp_f32_e32 v214, v214
	v_exp_f32_e32 v215, v215
	v_exp_f32_e32 v216, v216
	v_exp_f32_e32 v217, v217
	v_exp_f32_e32 v218, v218
	v_exp_f32_e32 v219, v219
	v_add_f32_e32 v212, 1.0, v212
	v_add_f32_e32 v213, 1.0, v213
	v_add_f32_e32 v214, 1.0, v214
	v_add_f32_e32 v215, 1.0, v215
	v_add_f32_e32 v216, 1.0, v216
	v_add_f32_e32 v217, 1.0, v217
	v_add_f32_e32 v218, 1.0, v218
	v_add_f32_e32 v219, 1.0, v219
	v_rcp_f32_e32 v212, v212
	v_rcp_f32_e32 v213, v213
	v_rcp_f32_e32 v214, v214
	v_rcp_f32_e32 v215, v215
	v_rcp_f32_e32 v216, v216
	v_rcp_f32_e32 v217, v217
	v_rcp_f32_e32 v218, v218
	v_rcp_f32_e32 v219, v219
	v_lshlrev_b32_e32 v164, 16, v168
	v_and_b32_e32 v165, 0xffff0000, v168
	v_lshlrev_b32_e32 v166, 16, v169
	v_and_b32_e32 v167, 0xffff0000, v169
	v_pk_fma_f32 v[94:95], v[94:95], v[212:213], v[164:165]
	v_pk_fma_f32 v[96:97], v[96:97], v[214:215], v[166:167]
	v_lshlrev_b32_e32 v168, 16, v170
	v_and_b32_e32 v169, 0xffff0000, v170
	v_lshlrev_b32_e32 v170, 16, v171
	v_and_b32_e32 v171, 0xffff0000, v171
	v_pk_fma_f32 v[90:91], v[90:91], v[216:217], v[168:169]
	v_pk_fma_f32 v[92:93], v[92:93], v[218:219], v[170:171]
	v_cvt_pk_bf16_f32 v212, v94, v95
	v_cvt_pk_bf16_f32 v213, v96, v97
	v_cvt_pk_bf16_f32 v214, v90, v91
	v_cvt_pk_bf16_f32 v215, v92, v93
	global_store_dwordx4 v[240:241], v[212:215], off
	v_lshlrev_b32_e32 v220, 16, v172
	v_and_b32_e32 v221, 0xffff0000, v172
	v_lshlrev_b32_e32 v222, 16, v173
	v_and_b32_e32 v223, 0xffff0000, v173
	v_lshlrev_b32_e32 v224, 16, v174
	v_and_b32_e32 v225, 0xffff0000, v174
	v_lshlrev_b32_e32 v226, 16, v175
	v_and_b32_e32 v227, 0xffff0000, v175
	v_add_f32_e32 v220, v204, v220
	v_add_f32_e32 v221, v205, v221
	v_add_f32_e32 v222, v206, v222
	v_add_f32_e32 v223, v207, v223
	v_add_f32_e32 v224, v208, v224
	v_add_f32_e32 v225, v209, v225
	v_add_f32_e32 v226, v210, v226
	v_add_f32_e32 v227, v211, v227
	v_mul_f32_e32 v220, 0xbfb8aa3b, v220
	v_mul_f32_e32 v221, 0xbfb8aa3b, v221
	v_mul_f32_e32 v222, 0xbfb8aa3b, v222
	v_mul_f32_e32 v223, 0xbfb8aa3b, v223
	v_mul_f32_e32 v224, 0xbfb8aa3b, v224
	v_mul_f32_e32 v225, 0xbfb8aa3b, v225
	v_mul_f32_e32 v226, 0xbfb8aa3b, v226
	v_mul_f32_e32 v227, 0xbfb8aa3b, v227
	v_exp_f32_e32 v220, v220
	v_exp_f32_e32 v221, v221
	v_exp_f32_e32 v222, v222
	v_exp_f32_e32 v223, v223
	v_exp_f32_e32 v224, v224
	v_exp_f32_e32 v225, v225
	v_exp_f32_e32 v226, v226
	v_exp_f32_e32 v227, v227
	v_add_f32_e32 v220, 1.0, v220
	v_add_f32_e32 v221, 1.0, v221
	v_add_f32_e32 v222, 1.0, v222
	v_add_f32_e32 v223, 1.0, v223
	v_add_f32_e32 v224, 1.0, v224
	v_add_f32_e32 v225, 1.0, v225
	v_add_f32_e32 v226, 1.0, v226
	v_add_f32_e32 v227, 1.0, v227
	v_rcp_f32_e32 v220, v220
	v_rcp_f32_e32 v221, v221
	v_rcp_f32_e32 v222, v222
	v_rcp_f32_e32 v223, v223
	v_rcp_f32_e32 v224, v224
	v_rcp_f32_e32 v225, v225
	v_rcp_f32_e32 v226, v226
	v_rcp_f32_e32 v227, v227
	v_lshlrev_b32_e32 v172, 16, v176
	v_and_b32_e32 v173, 0xffff0000, v176
	v_lshlrev_b32_e32 v174, 16, v177
	v_and_b32_e32 v175, 0xffff0000, v177
	v_pk_fma_f32 v[86:87], v[86:87], v[220:221], v[172:173]
	v_pk_fma_f32 v[88:89], v[88:89], v[222:223], v[174:175]
	v_lshlrev_b32_e32 v176, 16, v178
	v_and_b32_e32 v177, 0xffff0000, v178
	v_lshlrev_b32_e32 v178, 16, v179
	v_and_b32_e32 v179, 0xffff0000, v179
	v_pk_fma_f32 v[82:83], v[82:83], v[224:225], v[176:177]
	v_pk_fma_f32 v[84:85], v[84:85], v[226:227], v[178:179]
	v_cvt_pk_bf16_f32 v220, v86, v87
	v_cvt_pk_bf16_f32 v221, v88, v89
	v_cvt_pk_bf16_f32 v222, v82, v83
	v_cvt_pk_bf16_f32 v223, v84, v85
	global_store_dwordx4 v[240:241], v[220:223], off offset:256
	v_lshl_add_u64 v[240:241], v[240:241], 0, s[100:101]
	v_lshlrev_b32_e32 v212, 16, v180
	v_and_b32_e32 v213, 0xffff0000, v180
	v_lshlrev_b32_e32 v214, 16, v181
	v_and_b32_e32 v215, 0xffff0000, v181
	v_lshlrev_b32_e32 v216, 16, v182
	v_and_b32_e32 v217, 0xffff0000, v182
	v_lshlrev_b32_e32 v218, 16, v183
	v_and_b32_e32 v219, 0xffff0000, v183
	v_add_f32_e32 v212, v196, v212
	v_add_f32_e32 v213, v197, v213
	v_add_f32_e32 v214, v198, v214
	v_add_f32_e32 v215, v199, v215
	v_add_f32_e32 v216, v200, v216
	v_add_f32_e32 v217, v201, v217
	v_add_f32_e32 v218, v202, v218
	v_add_f32_e32 v219, v203, v219
	v_mul_f32_e32 v212, 0xbfb8aa3b, v212
	v_mul_f32_e32 v213, 0xbfb8aa3b, v213
	v_mul_f32_e32 v214, 0xbfb8aa3b, v214
	v_mul_f32_e32 v215, 0xbfb8aa3b, v215
	v_mul_f32_e32 v216, 0xbfb8aa3b, v216
	v_mul_f32_e32 v217, 0xbfb8aa3b, v217
	v_mul_f32_e32 v218, 0xbfb8aa3b, v218
	v_mul_f32_e32 v219, 0xbfb8aa3b, v219
	v_exp_f32_e32 v212, v212
	v_exp_f32_e32 v213, v213
	v_exp_f32_e32 v214, v214
	v_exp_f32_e32 v215, v215
	v_exp_f32_e32 v216, v216
	v_exp_f32_e32 v217, v217
	v_exp_f32_e32 v218, v218
	v_exp_f32_e32 v219, v219
	v_add_f32_e32 v212, 1.0, v212
; __device__ __forceinline__ unsigned cvt_pk_bf16(float lo, float hi) { unsigned r; asm volatile("v_cvt_pk_bf16_f32 %0, %1, %2" : "=v"(r) : "v"(lo), "v"(hi)); return r; }
; __device__ __forceinline__ float sigm(float x) { return __builtin_amdgcn_rcpf(1.f + __expf(-x)); }
;     __device__ __forceinline__ void operator()(const f32x4 (&acc)[2][2][4][2], const Unit& u, int wr, int wc, int fr, int fq) const {
;         const int row0 = u.pm * BM + wr * 64 + fr, col0 = u.pn * BM + wc * 32 + 8 * fq;
; #pragma unroll
;         for (int ai = 0; ai < 2; ++ai)
; #pragma unroll
;             for (int m = 0; m < 4; ++m) { const size_t r = (size_t)(row0 + ai * HALF + m * 16);
; #pragma unroll
;                 for (int bj = 0; bj < 2; ++bj) { const int c = col0 + bj * HALF;
;                     const v4u pg = *(const v4u*)(P + r * NINP + GTO + D + c); const f32x4 b0 = *(const f32x4*)(bg + D + c), b1 = *(const f32x4*)(bg + D + c + 4);
;                     const v4u tw = *(const v4u*)(TMP + r * D + c); const f32x4 t0 = (f32x4){__uint_as_float(tw.x << 16), __uint_as_float(tw.x & 0xffff0000u), __uint_as_float(tw.y << 16), __uint_as_float(tw.y & 0xffff0000u)}, t1 = (f32x4){__uint_as_float(tw.z << 16), __uint_as_float(tw.z & 0xffff0000u), __uint_as_float(tw.w << 16), __uint_as_float(tw.w & 0xffff0000u)};
;                     f32x4 g0, g1;
;                     g0[0] = sigm(__uint_as_float(pg.x << 16) + b0[0]); g0[1] = sigm(__uint_as_float(pg.x & 0xffff0000u) + b0[1]);
;                     g0[2] = sigm(__uint_as_float(pg.y << 16) + b0[2]); g0[3] = sigm(__uint_as_float(pg.y & 0xffff0000u) + b0[3]);
;                     g1[0] = sigm(__uint_as_float(pg.z << 16) + b1[0]); g1[1] = sigm(__uint_as_float(pg.z & 0xffff0000u) + b1[1]);
;                     g1[2] = sigm(__uint_as_float(pg.w << 16) + b1[2]); g1[3] = sigm(__uint_as_float(pg.w & 0xffff0000u) + b1[3]);
;                     const f32x4 v0 = t0 + g0 * acc[ai][bj][m][0], v1 = t1 + g1 * acc[ai][bj][m][1];
;                     v4u w; w.x = pg8::cvt_pk_bf16(v0[0], v0[1]); w.y = pg8::cvt_pk_bf16(v0[2], v0[3]); w.z = pg8::cvt_pk_bf16(v1[0], v1[1]); w.w = pg8::cvt_pk_bf16(v1[2], v1[3]);
;                     *(v4u*)(MRG + r * D + c) = w; } }
;     }
	v_add_f32_e32 v213, 1.0, v213
	v_add_f32_e32 v214, 1.0, v214
	v_add_f32_e32 v215, 1.0, v215
	v_add_f32_e32 v216, 1.0, v216
	v_add_f32_e32 v217, 1.0, v217
	v_add_f32_e32 v218, 1.0, v218
	v_add_f32_e32 v219, 1.0, v219
	v_rcp_f32_e32 v212, v212
	v_rcp_f32_e32 v213, v213
	v_rcp_f32_e32 v214, v214
	v_rcp_f32_e32 v215, v215
	v_rcp_f32_e32 v216, v216
	v_rcp_f32_e32 v217, v217
	v_rcp_f32_e32 v218, v218
	v_rcp_f32_e32 v219, v219
	v_lshlrev_b32_e32 v180, 16, v184
	v_and_b32_e32 v181, 0xffff0000, v184
	v_lshlrev_b32_e32 v182, 16, v185
	v_and_b32_e32 v183, 0xffff0000, v185
	v_pk_fma_f32 v[78:79], v[78:79], v[212:213], v[180:181]
	v_pk_fma_f32 v[80:81], v[80:81], v[214:215], v[182:183]
	v_lshlrev_b32_e32 v184, 16, v186
	v_and_b32_e32 v185, 0xffff0000, v186
	v_lshlrev_b32_e32 v186, 16, v187
	v_and_b32_e32 v187, 0xffff0000, v187
	v_pk_fma_f32 v[74:75], v[74:75], v[216:217], v[184:185]
	v_pk_fma_f32 v[76:77], v[76:77], v[218:219], v[186:187]
	v_cvt_pk_bf16_f32 v212, v78, v79
	v_cvt_pk_bf16_f32 v213, v80, v81
	v_cvt_pk_bf16_f32 v214, v74, v75
	v_cvt_pk_bf16_f32 v215, v76, v77
	global_store_dwordx4 v[240:241], v[212:215], off
	v_lshlrev_b32_e32 v220, 16, v188
	v_and_b32_e32 v221, 0xffff0000, v188
	v_lshlrev_b32_e32 v222, 16, v189
	v_and_b32_e32 v223, 0xffff0000, v189
	v_lshlrev_b32_e32 v224, 16, v190
	v_and_b32_e32 v225, 0xffff0000, v190
	v_lshlrev_b32_e32 v226, 16, v191
	v_and_b32_e32 v227, 0xffff0000, v191
	v_add_f32_e32 v220, v204, v220
	v_add_f32_e32 v221, v205, v221
	v_add_f32_e32 v222, v206, v222
	v_add_f32_e32 v223, v207, v223
	v_add_f32_e32 v224, v208, v224
	v_add_f32_e32 v225, v209, v225
	v_add_f32_e32 v226, v210, v226
	v_add_f32_e32 v227, v211, v227
	v_mul_f32_e32 v220, 0xbfb8aa3b, v220
	v_mul_f32_e32 v221, 0xbfb8aa3b, v221
	v_mul_f32_e32 v222, 0xbfb8aa3b, v222
	v_mul_f32_e32 v223, 0xbfb8aa3b, v223
	v_mul_f32_e32 v224, 0xbfb8aa3b, v224
	v_mul_f32_e32 v225, 0xbfb8aa3b, v225
	v_mul_f32_e32 v226, 0xbfb8aa3b, v226
	v_mul_f32_e32 v227, 0xbfb8aa3b, v227
	v_exp_f32_e32 v220, v220
	v_exp_f32_e32 v221, v221
	v_exp_f32_e32 v222, v222
	v_exp_f32_e32 v223, v223
	v_exp_f32_e32 v224, v224
	v_exp_f32_e32 v225, v225
	v_exp_f32_e32 v226, v226
	v_exp_f32_e32 v227, v227
	v_add_f32_e32 v220, 1.0, v220
	v_add_f32_e32 v221, 1.0, v221
	v_add_f32_e32 v222, 1.0, v222
	v_add_f32_e32 v223, 1.0, v223
	v_add_f32_e32 v224, 1.0, v224
	v_add_f32_e32 v225, 1.0, v225
	v_add_f32_e32 v226, 1.0, v226
	v_add_f32_e32 v227, 1.0, v227
	v_rcp_f32_e32 v220, v220
	v_rcp_f32_e32 v221, v221
	v_rcp_f32_e32 v222, v222
	v_rcp_f32_e32 v223, v223
	v_rcp_f32_e32 v224, v224
	v_rcp_f32_e32 v225, v225
	v_rcp_f32_e32 v226, v226
	v_rcp_f32_e32 v227, v227
	v_lshlrev_b32_e32 v188, 16, v192
	v_and_b32_e32 v189, 0xffff0000, v192
	v_lshlrev_b32_e32 v190, 16, v193
	v_and_b32_e32 v191, 0xffff0000, v193
	v_pk_fma_f32 v[70:71], v[70:71], v[220:221], v[188:189]
	v_pk_fma_f32 v[72:73], v[72:73], v[222:223], v[190:191]
	v_lshlrev_b32_e32 v192, 16, v194
	v_and_b32_e32 v193, 0xffff0000, v194
	v_lshlrev_b32_e32 v194, 16, v195
	v_and_b32_e32 v195, 0xffff0000, v195
	v_pk_fma_f32 v[66:67], v[66:67], v[224:225], v[192:193]
	v_pk_fma_f32 v[68:69], v[68:69], v[226:227], v[194:195]
	v_cvt_pk_bf16_f32 v220, v70, v71
	v_cvt_pk_bf16_f32 v221, v72, v73
	v_cvt_pk_bf16_f32 v222, v66, v67
	v_cvt_pk_bf16_f32 v223, v68, v69
	global_store_dwordx4 v[240:241], v[220:223], off offset:256
	global_load_dwordx4 v[164:167], v[244:245], off
	global_load_dwordx4 v[168:171], v[246:247], off
	global_load_dwordx4 v[172:175], v[244:245], off offset:256
	global_load_dwordx4 v[176:179], v[246:247], off offset:256
	v_lshl_add_u64 v[244:245], v[244:245], 0, s[98:99]
	v_lshl_add_u64 v[246:247], v[246:247], 0, s[100:101]
	global_load_dwordx4 v[180:183], v[244:245], off
	global_load_dwordx4 v[184:187], v[246:247], off
	global_load_dwordx4 v[188:191], v[244:245], off offset:256
	global_load_dwordx4 v[192:195], v[246:247], off offset:256
	s_waitcnt vmcnt(0)
	v_lshlrev_b32_e32 v212, 16, v164
	v_and_b32_e32 v213, 0xffff0000, v164
	v_lshlrev_b32_e32 v214, 16, v165
	v_and_b32_e32 v215, 0xffff0000, v165
	v_lshlrev_b32_e32 v216, 16, v166
	v_and_b32_e32 v217, 0xffff0000, v166
	v_lshlrev_b32_e32 v218, 16, v167
	v_and_b32_e32 v219, 0xffff0000, v167
	v_add_f32_e32 v212, v196, v212
	v_add_f32_e32 v213, v197, v213
	v_add_f32_e32 v214, v198, v214
	v_add_f32_e32 v215, v199, v215
	v_add_f32_e32 v216, v200, v216
	v_add_f32_e32 v217, v201, v217
	v_add_f32_e32 v218, v202, v218
	v_add_f32_e32 v219, v203, v219
	v_mul_f32_e32 v212, 0xbfb8aa3b, v212
	v_mul_f32_e32 v213, 0xbfb8aa3b, v213
	v_mul_f32_e32 v214, 0xbfb8aa3b, v214
	v_mul_f32_e32 v215, 0xbfb8aa3b, v215
	v_mul_f32_e32 v216, 0xbfb8aa3b, v216
	v_mul_f32_e32 v217, 0xbfb8aa3b, v217
	v_mul_f32_e32 v218, 0xbfb8aa3b, v218
	v_mul_f32_e32 v219, 0xbfb8aa3b, v219
	v_exp_f32_e32 v212, v212
	v_exp_f32_e32 v213, v213
	v_exp_f32_e32 v214, v214
	v_exp_f32_e32 v215, v215
	v_exp_f32_e32 v216, v216
	v_exp_f32_e32 v217, v217
	v_exp_f32_e32 v218, v218
	v_exp_f32_e32 v219, v219
	v_add_f32_e32 v212, 1.0, v212
	v_add_f32_e32 v213, 1.0, v213
	v_add_f32_e32 v214, 1.0, v214
	v_add_f32_e32 v215, 1.0, v215
	v_add_f32_e32 v216, 1.0, v216
	v_add_f32_e32 v217, 1.0, v217
	v_add_f32_e32 v218, 1.0, v218
	v_add_f32_e32 v219, 1.0, v219
	v_rcp_f32_e32 v212, v212
	v_rcp_f32_e32 v213, v213
	v_rcp_f32_e32 v214, v214
	v_rcp_f32_e32 v215, v215
	v_rcp_f32_e32 v216, v216
	v_rcp_f32_e32 v217, v217
	v_rcp_f32_e32 v218, v218
	v_rcp_f32_e32 v219, v219
	v_lshlrev_b32_e32 v164, 16, v168
	v_and_b32_e32 v165, 0xffff0000, v168
	v_lshlrev_b32_e32 v166, 16, v169
	v_and_b32_e32 v167, 0xffff0000, v169
	v_pk_fma_f32 v[62:63], v[62:63], v[212:213], v[164:165]
; __device__ __forceinline__ unsigned cvt_pk_bf16(float lo, float hi) { unsigned r; asm volatile("v_cvt_pk_bf16_f32 %0, %1, %2" : "=v"(r) : "v"(lo), "v"(hi)); return r; }
; __device__ __forceinline__ float sigm(float x) { return __builtin_amdgcn_rcpf(1.f + __expf(-x)); }
;     __device__ __forceinline__ void operator()(const f32x4 (&acc)[2][2][4][2], const Unit& u, int wr, int wc, int fr, int fq) const {
;         const int row0 = u.pm * BM + wr * 64 + fr, col0 = u.pn * BM + wc * 32 + 8 * fq;
; #pragma unroll
;         for (int ai = 0; ai < 2; ++ai)
; #pragma unroll
;             for (int m = 0; m < 4; ++m) { const size_t r = (size_t)(row0 + ai * HALF + m * 16);
; #pragma unroll
;                 for (int bj = 0; bj < 2; ++bj) { const int c = col0 + bj * HALF;
;                     const v4u pg = *(const v4u*)(P + r * NINP + GTO + D + c); const f32x4 b0 = *(const f32x4*)(bg + D + c), b1 = *(const f32x4*)(bg + D + c + 4);
;                     const v4u tw = *(const v4u*)(TMP + r * D + c); const f32x4 t0 = (f32x4){__uint_as_float(tw.x << 16), __uint_as_float(tw.x & 0xffff0000u), __uint_as_float(tw.y << 16), __uint_as_float(tw.y & 0xffff0000u)}, t1 = (f32x4){__uint_as_float(tw.z << 16), __uint_as_float(tw.z & 0xffff0000u), __uint_as_float(tw.w << 16), __uint_as_float(tw.w & 0xffff0000u)};
;                     f32x4 g0, g1;
;                     g0[0] = sigm(__uint_as_float(pg.x << 16) + b0[0]); g0[1] = sigm(__uint_as_float(pg.x & 0xffff0000u) + b0[1]);
;                     g0[2] = sigm(__uint_as_float(pg.y << 16) + b0[2]); g0[3] = sigm(__uint_as_float(pg.y & 0xffff0000u) + b0[3]);
;                     g1[0] = sigm(__uint_as_float(pg.z << 16) + b1[0]); g1[1] = sigm(__uint_as_float(pg.z & 0xffff0000u) + b1[1]);
;                     g1[2] = sigm(__uint_as_float(pg.w << 16) + b1[2]); g1[3] = sigm(__uint_as_float(pg.w & 0xffff0000u) + b1[3]);
;                     const f32x4 v0 = t0 + g0 * acc[ai][bj][m][0], v1 = t1 + g1 * acc[ai][bj][m][1];
;                     v4u w; w.x = pg8::cvt_pk_bf16(v0[0], v0[1]); w.y = pg8::cvt_pk_bf16(v0[2], v0[3]); w.z = pg8::cvt_pk_bf16(v1[0], v1[1]); w.w = pg8::cvt_pk_bf16(v1[2], v1[3]);
;                     *(v4u*)(MRG + r * D + c) = w; } }
;     }
	v_pk_fma_f32 v[64:65], v[64:65], v[214:215], v[166:167]
	v_lshlrev_b32_e32 v168, 16, v170
	v_and_b32_e32 v169, 0xffff0000, v170
	v_lshlrev_b32_e32 v170, 16, v171
	v_and_b32_e32 v171, 0xffff0000, v171
	v_pk_fma_f32 v[58:59], v[58:59], v[216:217], v[168:169]
	v_pk_fma_f32 v[60:61], v[60:61], v[218:219], v[170:171]
	v_cvt_pk_bf16_f32 v212, v62, v63
	v_cvt_pk_bf16_f32 v213, v64, v65
	v_cvt_pk_bf16_f32 v214, v58, v59
	v_cvt_pk_bf16_f32 v215, v60, v61
	global_store_dwordx4 v[150:151], v[212:215], off
	v_lshlrev_b32_e32 v220, 16, v172
	v_and_b32_e32 v221, 0xffff0000, v172
	v_lshlrev_b32_e32 v222, 16, v173
	v_and_b32_e32 v223, 0xffff0000, v173
	v_lshlrev_b32_e32 v224, 16, v174
	v_and_b32_e32 v225, 0xffff0000, v174
	v_lshlrev_b32_e32 v226, 16, v175
	v_and_b32_e32 v227, 0xffff0000, v175
	v_add_f32_e32 v220, v204, v220
	v_add_f32_e32 v221, v205, v221
	v_add_f32_e32 v222, v206, v222
	v_add_f32_e32 v223, v207, v223
	v_add_f32_e32 v224, v208, v224
	v_add_f32_e32 v225, v209, v225
	v_add_f32_e32 v226, v210, v226
	v_add_f32_e32 v227, v211, v227
	v_mul_f32_e32 v220, 0xbfb8aa3b, v220
	v_mul_f32_e32 v221, 0xbfb8aa3b, v221
	v_mul_f32_e32 v222, 0xbfb8aa3b, v222
	v_mul_f32_e32 v223, 0xbfb8aa3b, v223
	v_mul_f32_e32 v224, 0xbfb8aa3b, v224
	v_mul_f32_e32 v225, 0xbfb8aa3b, v225
	v_mul_f32_e32 v226, 0xbfb8aa3b, v226
	v_mul_f32_e32 v227, 0xbfb8aa3b, v227
	v_exp_f32_e32 v220, v220
	v_exp_f32_e32 v221, v221
	v_exp_f32_e32 v222, v222
	v_exp_f32_e32 v223, v223
	v_exp_f32_e32 v224, v224
	v_exp_f32_e32 v225, v225
	v_exp_f32_e32 v226, v226
	v_exp_f32_e32 v227, v227
	v_add_f32_e32 v220, 1.0, v220
	v_add_f32_e32 v221, 1.0, v221
	v_add_f32_e32 v222, 1.0, v222
	v_add_f32_e32 v223, 1.0, v223
	v_add_f32_e32 v224, 1.0, v224
	v_add_f32_e32 v225, 1.0, v225
	v_add_f32_e32 v226, 1.0, v226
	v_add_f32_e32 v227, 1.0, v227
	v_rcp_f32_e32 v220, v220
	v_rcp_f32_e32 v221, v221
	v_rcp_f32_e32 v222, v222
	v_rcp_f32_e32 v223, v223
	v_rcp_f32_e32 v224, v224
	v_rcp_f32_e32 v225, v225
	v_rcp_f32_e32 v226, v226
	v_rcp_f32_e32 v227, v227
	v_lshlrev_b32_e32 v172, 16, v176
	v_and_b32_e32 v173, 0xffff0000, v176
	v_lshlrev_b32_e32 v174, 16, v177
	v_and_b32_e32 v175, 0xffff0000, v177
	v_pk_fma_f32 v[54:55], v[54:55], v[220:221], v[172:173]
	v_pk_fma_f32 v[56:57], v[56:57], v[222:223], v[174:175]
	v_lshlrev_b32_e32 v176, 16, v178
	v_and_b32_e32 v177, 0xffff0000, v178
	v_lshlrev_b32_e32 v178, 16, v179
	v_and_b32_e32 v179, 0xffff0000, v179
	v_pk_fma_f32 v[50:51], v[50:51], v[224:225], v[176:177]
	v_pk_fma_f32 v[52:53], v[52:53], v[226:227], v[178:179]
	v_cvt_pk_bf16_f32 v220, v54, v55
	v_cvt_pk_bf16_f32 v221, v56, v57
	v_cvt_pk_bf16_f32 v222, v50, v51
	v_cvt_pk_bf16_f32 v223, v52, v53
	global_store_dwordx4 v[150:151], v[220:223], off offset:256
	v_lshl_add_u64 v[150:151], v[150:151], 0, s[100:101]
	v_lshlrev_b32_e32 v212, 16, v180
	v_and_b32_e32 v213, 0xffff0000, v180
	v_lshlrev_b32_e32 v214, 16, v181
	v_and_b32_e32 v215, 0xffff0000, v181
	v_lshlrev_b32_e32 v216, 16, v182
	v_and_b32_e32 v217, 0xffff0000, v182
	v_lshlrev_b32_e32 v218, 16, v183
	v_and_b32_e32 v219, 0xffff0000, v183
	v_add_f32_e32 v212, v196, v212
	v_add_f32_e32 v213, v197, v213
	v_add_f32_e32 v214, v198, v214
	v_add_f32_e32 v215, v199, v215
	v_add_f32_e32 v216, v200, v216
	v_add_f32_e32 v217, v201, v217
	v_add_f32_e32 v218, v202, v218
	v_add_f32_e32 v219, v203, v219
	v_mul_f32_e32 v212, 0xbfb8aa3b, v212
	v_mul_f32_e32 v213, 0xbfb8aa3b, v213
	v_mul_f32_e32 v214, 0xbfb8aa3b, v214
	v_mul_f32_e32 v215, 0xbfb8aa3b, v215
	v_mul_f32_e32 v216, 0xbfb8aa3b, v216
	v_mul_f32_e32 v217, 0xbfb8aa3b, v217
	v_mul_f32_e32 v218, 0xbfb8aa3b, v218
	v_mul_f32_e32 v219, 0xbfb8aa3b, v219
	v_exp_f32_e32 v212, v212
	v_exp_f32_e32 v213, v213
	v_exp_f32_e32 v214, v214
	v_exp_f32_e32 v215, v215
	v_exp_f32_e32 v216, v216
	v_exp_f32_e32 v217, v217
	v_exp_f32_e32 v218, v218
	v_exp_f32_e32 v219, v219
	v_add_f32_e32 v212, 1.0, v212
	v_add_f32_e32 v213, 1.0, v213
	v_add_f32_e32 v214, 1.0, v214
	v_add_f32_e32 v215, 1.0, v215
	v_add_f32_e32 v216, 1.0, v216
	v_add_f32_e32 v217, 1.0, v217
	v_add_f32_e32 v218, 1.0, v218
	v_add_f32_e32 v219, 1.0, v219
	v_rcp_f32_e32 v212, v212
	v_rcp_f32_e32 v213, v213
	v_rcp_f32_e32 v214, v214
	v_rcp_f32_e32 v215, v215
	v_rcp_f32_e32 v216, v216
	v_rcp_f32_e32 v217, v217
	v_rcp_f32_e32 v218, v218
	v_rcp_f32_e32 v219, v219
	v_lshlrev_b32_e32 v180, 16, v184
	v_and_b32_e32 v181, 0xffff0000, v184
	v_lshlrev_b32_e32 v182, 16, v185
	v_and_b32_e32 v183, 0xffff0000, v185
	v_pk_fma_f32 v[46:47], v[46:47], v[212:213], v[180:181]
	v_pk_fma_f32 v[48:49], v[48:49], v[214:215], v[182:183]
	v_lshlrev_b32_e32 v184, 16, v186
	v_and_b32_e32 v185, 0xffff0000, v186
	v_lshlrev_b32_e32 v186, 16, v187
	v_and_b32_e32 v187, 0xffff0000, v187
	v_pk_fma_f32 v[42:43], v[42:43], v[216:217], v[184:185]
	v_pk_fma_f32 v[44:45], v[44:45], v[218:219], v[186:187]
	v_cvt_pk_bf16_f32 v212, v46, v47
	v_cvt_pk_bf16_f32 v213, v48, v49
	v_cvt_pk_bf16_f32 v214, v42, v43
	v_cvt_pk_bf16_f32 v215, v44, v45
	global_store_dwordx4 v[150:151], v[212:215], off
	v_lshlrev_b32_e32 v220, 16, v188
	v_and_b32_e32 v221, 0xffff0000, v188
	v_lshlrev_b32_e32 v222, 16, v189
	v_and_b32_e32 v223, 0xffff0000, v189
	v_lshlrev_b32_e32 v224, 16, v190
	v_and_b32_e32 v225, 0xffff0000, v190
	v_lshlrev_b32_e32 v226, 16, v191
	v_and_b32_e32 v227, 0xffff0000, v191
	v_add_f32_e32 v220, v204, v220
	v_add_f32_e32 v221, v205, v221
	v_add_f32_e32 v222, v206, v222
	v_add_f32_e32 v223, v207, v223
	v_add_f32_e32 v224, v208, v224
	v_add_f32_e32 v225, v209, v225
	v_add_f32_e32 v226, v210, v226
	v_add_f32_e32 v227, v211, v227
	v_mul_f32_e32 v220, 0xbfb8aa3b, v220
	v_mul_f32_e32 v221, 0xbfb8aa3b, v221
	v_mul_f32_e32 v222, 0xbfb8aa3b, v222
; __device__ __forceinline__ unsigned cvt_pk_bf16(float lo, float hi) { unsigned r; asm volatile("v_cvt_pk_bf16_f32 %0, %1, %2" : "=v"(r) : "v"(lo), "v"(hi)); return r; }
; __device__ __forceinline__ float sigm(float x) { return __builtin_amdgcn_rcpf(1.f + __expf(-x)); }
;     __device__ __forceinline__ void operator()(const f32x4 (&acc)[2][2][4][2], const Unit& u, int wr, int wc, int fr, int fq) const {
;         const int row0 = u.pm * BM + wr * 64 + fr, col0 = u.pn * BM + wc * 32 + 8 * fq;
; #pragma unroll
;         for (int ai = 0; ai < 2; ++ai)
; #pragma unroll
;             for (int m = 0; m < 4; ++m) { const size_t r = (size_t)(row0 + ai * HALF + m * 16);
; #pragma unroll
;                 for (int bj = 0; bj < 2; ++bj) { const int c = col0 + bj * HALF;
;                     const v4u pg = *(const v4u*)(P + r * NINP + GTO + D + c); const f32x4 b0 = *(const f32x4*)(bg + D + c), b1 = *(const f32x4*)(bg + D + c + 4);
;                     const v4u tw = *(const v4u*)(TMP + r * D + c); const f32x4 t0 = (f32x4){__uint_as_float(tw.x << 16), __uint_as_float(tw.x & 0xffff0000u), __uint_as_float(tw.y << 16), __uint_as_float(tw.y & 0xffff0000u)}, t1 = (f32x4){__uint_as_float(tw.z << 16), __uint_as_float(tw.z & 0xffff0000u), __uint_as_float(tw.w << 16), __uint_as_float(tw.w & 0xffff0000u)};
;                     f32x4 g0, g1;
;                     g0[0] = sigm(__uint_as_float(pg.x << 16) + b0[0]); g0[1] = sigm(__uint_as_float(pg.x & 0xffff0000u) + b0[1]);
;                     g0[2] = sigm(__uint_as_float(pg.y << 16) + b0[2]); g0[3] = sigm(__uint_as_float(pg.y & 0xffff0000u) + b0[3]);
;                     g1[0] = sigm(__uint_as_float(pg.z << 16) + b1[0]); g1[1] = sigm(__uint_as_float(pg.z & 0xffff0000u) + b1[1]);
;                     g1[2] = sigm(__uint_as_float(pg.w << 16) + b1[2]); g1[3] = sigm(__uint_as_float(pg.w & 0xffff0000u) + b1[3]);
;                     const f32x4 v0 = t0 + g0 * acc[ai][bj][m][0], v1 = t1 + g1 * acc[ai][bj][m][1];
;                     v4u w; w.x = pg8::cvt_pk_bf16(v0[0], v0[1]); w.y = pg8::cvt_pk_bf16(v0[2], v0[3]); w.z = pg8::cvt_pk_bf16(v1[0], v1[1]); w.w = pg8::cvt_pk_bf16(v1[2], v1[3]);
;                     *(v4u*)(MRG + r * D + c) = w; } }
;     }
	v_mul_f32_e32 v223, 0xbfb8aa3b, v223
	v_mul_f32_e32 v224, 0xbfb8aa3b, v224
	v_mul_f32_e32 v225, 0xbfb8aa3b, v225
	v_mul_f32_e32 v226, 0xbfb8aa3b, v226
	v_mul_f32_e32 v227, 0xbfb8aa3b, v227
	v_exp_f32_e32 v220, v220
	v_exp_f32_e32 v221, v221
	v_exp_f32_e32 v222, v222
	v_exp_f32_e32 v223, v223
	v_exp_f32_e32 v224, v224
	v_exp_f32_e32 v225, v225
	v_exp_f32_e32 v226, v226
	v_exp_f32_e32 v227, v227
	v_add_f32_e32 v220, 1.0, v220
	v_add_f32_e32 v221, 1.0, v221
	v_add_f32_e32 v222, 1.0, v222
	v_add_f32_e32 v223, 1.0, v223
	v_add_f32_e32 v224, 1.0, v224
	v_add_f32_e32 v225, 1.0, v225
	v_add_f32_e32 v226, 1.0, v226
	v_add_f32_e32 v227, 1.0, v227
	v_rcp_f32_e32 v220, v220
	v_rcp_f32_e32 v221, v221
	v_rcp_f32_e32 v222, v222
	v_rcp_f32_e32 v223, v223
	v_rcp_f32_e32 v224, v224
	v_rcp_f32_e32 v225, v225
	v_rcp_f32_e32 v226, v226
	v_rcp_f32_e32 v227, v227
	v_lshlrev_b32_e32 v188, 16, v192
	v_and_b32_e32 v189, 0xffff0000, v192
	v_lshlrev_b32_e32 v190, 16, v193
	v_and_b32_e32 v191, 0xffff0000, v193
	v_pk_fma_f32 v[38:39], v[38:39], v[220:221], v[188:189]
	v_pk_fma_f32 v[40:41], v[40:41], v[222:223], v[190:191]
	v_lshlrev_b32_e32 v192, 16, v194
	v_and_b32_e32 v193, 0xffff0000, v194
	v_lshlrev_b32_e32 v194, 16, v195
	v_and_b32_e32 v195, 0xffff0000, v195
	v_pk_fma_f32 v[34:35], v[34:35], v[224:225], v[192:193]
	v_pk_fma_f32 v[36:37], v[36:37], v[226:227], v[194:195]
	v_cvt_pk_bf16_f32 v220, v38, v39
	v_cvt_pk_bf16_f32 v221, v40, v41
	v_cvt_pk_bf16_f32 v222, v34, v35
	v_cvt_pk_bf16_f32 v223, v36, v37
	global_store_dwordx4 v[150:151], v[220:223], off offset:256
	v_lshl_add_u64 v[244:245], v[244:245], 0, s[98:99]
	v_lshl_add_u64 v[246:247], v[246:247], 0, s[100:101]
	global_load_dwordx4 v[164:167], v[244:245], off
	global_load_dwordx4 v[168:171], v[246:247], off
	global_load_dwordx4 v[172:175], v[244:245], off offset:256
	global_load_dwordx4 v[176:179], v[246:247], off offset:256
	v_lshl_add_u64 v[244:245], v[244:245], 0, s[98:99]
	v_lshl_add_u64 v[246:247], v[246:247], 0, s[100:101]
	global_load_dwordx4 v[180:183], v[244:245], off
	global_load_dwordx4 v[184:187], v[246:247], off
	global_load_dwordx4 v[188:191], v[244:245], off offset:256
	global_load_dwordx4 v[192:195], v[246:247], off offset:256
	s_waitcnt vmcnt(0)
	v_lshl_add_u64 v[150:151], v[150:151], 0, s[100:101]
	v_lshlrev_b32_e32 v212, 16, v164
	v_and_b32_e32 v213, 0xffff0000, v164
	v_lshlrev_b32_e32 v214, 16, v165
	v_and_b32_e32 v215, 0xffff0000, v165
	v_lshlrev_b32_e32 v216, 16, v166
	v_and_b32_e32 v217, 0xffff0000, v166
	v_lshlrev_b32_e32 v218, 16, v167
	v_and_b32_e32 v219, 0xffff0000, v167
	v_add_f32_e32 v212, v196, v212
	v_add_f32_e32 v213, v197, v213
	v_add_f32_e32 v214, v198, v214
	v_add_f32_e32 v215, v199, v215
	v_add_f32_e32 v216, v200, v216
	v_add_f32_e32 v217, v201, v217
	v_add_f32_e32 v218, v202, v218
	v_add_f32_e32 v219, v203, v219
	v_mul_f32_e32 v212, 0xbfb8aa3b, v212
	v_mul_f32_e32 v213, 0xbfb8aa3b, v213
	v_mul_f32_e32 v214, 0xbfb8aa3b, v214
	v_mul_f32_e32 v215, 0xbfb8aa3b, v215
	v_mul_f32_e32 v216, 0xbfb8aa3b, v216
	v_mul_f32_e32 v217, 0xbfb8aa3b, v217
	v_mul_f32_e32 v218, 0xbfb8aa3b, v218
	v_mul_f32_e32 v219, 0xbfb8aa3b, v219
	v_exp_f32_e32 v212, v212
	v_exp_f32_e32 v213, v213
	v_exp_f32_e32 v214, v214
	v_exp_f32_e32 v215, v215
	v_exp_f32_e32 v216, v216
	v_exp_f32_e32 v217, v217
	v_exp_f32_e32 v218, v218
	v_exp_f32_e32 v219, v219
	v_add_f32_e32 v212, 1.0, v212
	v_add_f32_e32 v213, 1.0, v213
	v_add_f32_e32 v214, 1.0, v214
	v_add_f32_e32 v215, 1.0, v215
	v_add_f32_e32 v216, 1.0, v216
	v_add_f32_e32 v217, 1.0, v217
	v_add_f32_e32 v218, 1.0, v218
	v_add_f32_e32 v219, 1.0, v219
	v_rcp_f32_e32 v212, v212
	v_rcp_f32_e32 v213, v213
	v_rcp_f32_e32 v214, v214
	v_rcp_f32_e32 v215, v215
	v_rcp_f32_e32 v216, v216
	v_rcp_f32_e32 v217, v217
	v_rcp_f32_e32 v218, v218
	v_rcp_f32_e32 v219, v219
	v_lshlrev_b32_e32 v164, 16, v168
	v_and_b32_e32 v165, 0xffff0000, v168
	v_lshlrev_b32_e32 v166, 16, v169
	v_and_b32_e32 v167, 0xffff0000, v169
	v_pk_fma_f32 v[30:31], v[30:31], v[212:213], v[164:165]
	v_pk_fma_f32 v[32:33], v[32:33], v[214:215], v[166:167]
	v_lshlrev_b32_e32 v168, 16, v170
	v_and_b32_e32 v169, 0xffff0000, v170
	v_lshlrev_b32_e32 v170, 16, v171
	v_and_b32_e32 v171, 0xffff0000, v171
	v_pk_fma_f32 v[26:27], v[26:27], v[216:217], v[168:169]
	v_pk_fma_f32 v[28:29], v[28:29], v[218:219], v[170:171]
	v_cvt_pk_bf16_f32 v212, v30, v31
	v_cvt_pk_bf16_f32 v213, v32, v33
	v_cvt_pk_bf16_f32 v214, v26, v27
	v_cvt_pk_bf16_f32 v215, v28, v29
	global_store_dwordx4 v[150:151], v[212:215], off
	v_lshlrev_b32_e32 v220, 16, v172
	v_and_b32_e32 v221, 0xffff0000, v172
	v_lshlrev_b32_e32 v222, 16, v173
	v_and_b32_e32 v223, 0xffff0000, v173
	v_lshlrev_b32_e32 v224, 16, v174
	v_and_b32_e32 v225, 0xffff0000, v174
	v_lshlrev_b32_e32 v226, 16, v175
	v_and_b32_e32 v227, 0xffff0000, v175
	v_add_f32_e32 v220, v204, v220
	v_add_f32_e32 v221, v205, v221
	v_add_f32_e32 v222, v206, v222
	v_add_f32_e32 v223, v207, v223
	v_add_f32_e32 v224, v208, v224
	v_add_f32_e32 v225, v209, v225
	v_add_f32_e32 v226, v210, v226
	v_add_f32_e32 v227, v211, v227
	v_mul_f32_e32 v220, 0xbfb8aa3b, v220
	v_mul_f32_e32 v221, 0xbfb8aa3b, v221
	v_mul_f32_e32 v222, 0xbfb8aa3b, v222
	v_mul_f32_e32 v223, 0xbfb8aa3b, v223
	v_mul_f32_e32 v224, 0xbfb8aa3b, v224
	v_mul_f32_e32 v225, 0xbfb8aa3b, v225
	v_mul_f32_e32 v226, 0xbfb8aa3b, v226
	v_mul_f32_e32 v227, 0xbfb8aa3b, v227
	v_exp_f32_e32 v220, v220
	v_exp_f32_e32 v221, v221
	v_exp_f32_e32 v222, v222
	v_exp_f32_e32 v223, v223
	v_exp_f32_e32 v224, v224
	v_exp_f32_e32 v225, v225
	v_exp_f32_e32 v226, v226
	v_exp_f32_e32 v227, v227
	v_add_f32_e32 v220, 1.0, v220
	v_add_f32_e32 v221, 1.0, v221
	v_add_f32_e32 v222, 1.0, v222
; __device__ __forceinline__ unsigned cvt_pk_bf16(float lo, float hi) { unsigned r; asm volatile("v_cvt_pk_bf16_f32 %0, %1, %2" : "=v"(r) : "v"(lo), "v"(hi)); return r; }
; __device__ __forceinline__ float sigm(float x) { return __builtin_amdgcn_rcpf(1.f + __expf(-x)); }
;     __device__ __forceinline__ void operator()(const f32x4 (&acc)[2][2][4][2], const Unit& u, int wr, int wc, int fr, int fq) const {
;         const int row0 = u.pm * BM + wr * 64 + fr, col0 = u.pn * BM + wc * 32 + 8 * fq;
; #pragma unroll
;         for (int ai = 0; ai < 2; ++ai)
; #pragma unroll
;             for (int m = 0; m < 4; ++m) { const size_t r = (size_t)(row0 + ai * HALF + m * 16);
; #pragma unroll
;                 for (int bj = 0; bj < 2; ++bj) { const int c = col0 + bj * HALF;
;                     const v4u pg = *(const v4u*)(P + r * NINP + GTO + D + c); const f32x4 b0 = *(const f32x4*)(bg + D + c), b1 = *(const f32x4*)(bg + D + c + 4);
;                     const v4u tw = *(const v4u*)(TMP + r * D + c); const f32x4 t0 = (f32x4){__uint_as_float(tw.x << 16), __uint_as_float(tw.x & 0xffff0000u), __uint_as_float(tw.y << 16), __uint_as_float(tw.y & 0xffff0000u)}, t1 = (f32x4){__uint_as_float(tw.z << 16), __uint_as_float(tw.z & 0xffff0000u), __uint_as_float(tw.w << 16), __uint_as_float(tw.w & 0xffff0000u)};
;                     f32x4 g0, g1;
;                     g0[0] = sigm(__uint_as_float(pg.x << 16) + b0[0]); g0[1] = sigm(__uint_as_float(pg.x & 0xffff0000u) + b0[1]);
;                     g0[2] = sigm(__uint_as_float(pg.y << 16) + b0[2]); g0[3] = sigm(__uint_as_float(pg.y & 0xffff0000u) + b0[3]);
;                     g1[0] = sigm(__uint_as_float(pg.z << 16) + b1[0]); g1[1] = sigm(__uint_as_float(pg.z & 0xffff0000u) + b1[1]);
;                     g1[2] = sigm(__uint_as_float(pg.w << 16) + b1[2]); g1[3] = sigm(__uint_as_float(pg.w & 0xffff0000u) + b1[3]);
;                     const f32x4 v0 = t0 + g0 * acc[ai][bj][m][0], v1 = t1 + g1 * acc[ai][bj][m][1];
;                     v4u w; w.x = pg8::cvt_pk_bf16(v0[0], v0[1]); w.y = pg8::cvt_pk_bf16(v0[2], v0[3]); w.z = pg8::cvt_pk_bf16(v1[0], v1[1]); w.w = pg8::cvt_pk_bf16(v1[2], v1[3]);
;                     *(v4u*)(MRG + r * D + c) = w; } }
;     }
	v_add_f32_e32 v223, 1.0, v223
	v_add_f32_e32 v224, 1.0, v224
	v_add_f32_e32 v225, 1.0, v225
	v_add_f32_e32 v226, 1.0, v226
	v_add_f32_e32 v227, 1.0, v227
	v_rcp_f32_e32 v220, v220
	v_rcp_f32_e32 v221, v221
	v_rcp_f32_e32 v222, v222
	v_rcp_f32_e32 v223, v223
	v_rcp_f32_e32 v224, v224
	v_rcp_f32_e32 v225, v225
	v_rcp_f32_e32 v226, v226
	v_rcp_f32_e32 v227, v227
	v_lshlrev_b32_e32 v172, 16, v176
	v_and_b32_e32 v173, 0xffff0000, v176
	v_lshlrev_b32_e32 v174, 16, v177
	v_and_b32_e32 v175, 0xffff0000, v177
	v_pk_fma_f32 v[22:23], v[22:23], v[220:221], v[172:173]
	v_pk_fma_f32 v[24:25], v[24:25], v[222:223], v[174:175]
	v_lshlrev_b32_e32 v176, 16, v178
	v_and_b32_e32 v177, 0xffff0000, v178
	v_lshlrev_b32_e32 v178, 16, v179
	v_and_b32_e32 v179, 0xffff0000, v179
	v_pk_fma_f32 v[18:19], v[18:19], v[224:225], v[176:177]
	v_pk_fma_f32 v[20:21], v[20:21], v[226:227], v[178:179]
	v_cvt_pk_bf16_f32 v220, v22, v23
	v_cvt_pk_bf16_f32 v221, v24, v25
	v_cvt_pk_bf16_f32 v222, v18, v19
	v_cvt_pk_bf16_f32 v223, v20, v21
	global_store_dwordx4 v[150:151], v[220:223], off offset:256
	v_lshl_add_u64 v[150:151], v[150:151], 0, s[100:101]
	v_lshlrev_b32_e32 v212, 16, v180
	v_and_b32_e32 v213, 0xffff0000, v180
	v_lshlrev_b32_e32 v214, 16, v181
	v_and_b32_e32 v215, 0xffff0000, v181
	v_lshlrev_b32_e32 v216, 16, v182
	v_and_b32_e32 v217, 0xffff0000, v182
	v_lshlrev_b32_e32 v218, 16, v183
	v_and_b32_e32 v219, 0xffff0000, v183
	v_add_f32_e32 v212, v196, v212
	v_add_f32_e32 v213, v197, v213
	v_add_f32_e32 v214, v198, v214
	v_add_f32_e32 v215, v199, v215
	v_add_f32_e32 v216, v200, v216
	v_add_f32_e32 v217, v201, v217
	v_add_f32_e32 v218, v202, v218
	v_add_f32_e32 v219, v203, v219
	v_mul_f32_e32 v212, 0xbfb8aa3b, v212
	v_mul_f32_e32 v213, 0xbfb8aa3b, v213
	v_mul_f32_e32 v214, 0xbfb8aa3b, v214
	v_mul_f32_e32 v215, 0xbfb8aa3b, v215
	v_mul_f32_e32 v216, 0xbfb8aa3b, v216
	v_mul_f32_e32 v217, 0xbfb8aa3b, v217
	v_mul_f32_e32 v218, 0xbfb8aa3b, v218
	v_mul_f32_e32 v219, 0xbfb8aa3b, v219
	v_exp_f32_e32 v212, v212
	v_exp_f32_e32 v213, v213
	v_exp_f32_e32 v214, v214
	v_exp_f32_e32 v215, v215
	v_exp_f32_e32 v216, v216
	v_exp_f32_e32 v217, v217
	v_exp_f32_e32 v218, v218
	v_exp_f32_e32 v219, v219
	v_add_f32_e32 v212, 1.0, v212
	v_add_f32_e32 v213, 1.0, v213
	v_add_f32_e32 v214, 1.0, v214
	v_add_f32_e32 v215, 1.0, v215
	v_add_f32_e32 v216, 1.0, v216
	v_add_f32_e32 v217, 1.0, v217
	v_add_f32_e32 v218, 1.0, v218
	v_add_f32_e32 v219, 1.0, v219
	v_rcp_f32_e32 v212, v212
	v_rcp_f32_e32 v213, v213
	v_rcp_f32_e32 v214, v214
	v_rcp_f32_e32 v215, v215
	v_rcp_f32_e32 v216, v216
	v_rcp_f32_e32 v217, v217
	v_rcp_f32_e32 v218, v218
	v_rcp_f32_e32 v219, v219
	v_lshlrev_b32_e32 v180, 16, v184
	v_and_b32_e32 v181, 0xffff0000, v184
	v_lshlrev_b32_e32 v182, 16, v185
	v_and_b32_e32 v183, 0xffff0000, v185
	v_pk_fma_f32 v[14:15], v[14:15], v[212:213], v[180:181]
	v_pk_fma_f32 v[16:17], v[16:17], v[214:215], v[182:183]
	v_lshlrev_b32_e32 v184, 16, v186
	v_and_b32_e32 v185, 0xffff0000, v186
	v_lshlrev_b32_e32 v186, 16, v187
	v_and_b32_e32 v187, 0xffff0000, v187
	v_pk_fma_f32 v[10:11], v[10:11], v[216:217], v[184:185]
	v_pk_fma_f32 v[12:13], v[12:13], v[218:219], v[186:187]
	v_cvt_pk_bf16_f32 v212, v14, v15
	v_cvt_pk_bf16_f32 v213, v16, v17
	v_cvt_pk_bf16_f32 v214, v10, v11
	v_cvt_pk_bf16_f32 v215, v12, v13
	global_store_dwordx4 v[150:151], v[212:215], off
	v_lshlrev_b32_e32 v220, 16, v188
	v_and_b32_e32 v221, 0xffff0000, v188
	v_lshlrev_b32_e32 v222, 16, v189
	v_and_b32_e32 v223, 0xffff0000, v189
	v_lshlrev_b32_e32 v224, 16, v190
	v_and_b32_e32 v225, 0xffff0000, v190
	v_lshlrev_b32_e32 v226, 16, v191
	v_and_b32_e32 v227, 0xffff0000, v191
	v_add_f32_e32 v220, v204, v220
	v_add_f32_e32 v221, v205, v221
	v_add_f32_e32 v222, v206, v222
	v_add_f32_e32 v223, v207, v223
	v_add_f32_e32 v224, v208, v224
	v_add_f32_e32 v225, v209, v225
	v_add_f32_e32 v226, v210, v226
	v_add_f32_e32 v227, v211, v227
	v_mul_f32_e32 v220, 0xbfb8aa3b, v220
	v_mul_f32_e32 v221, 0xbfb8aa3b, v221
	v_mul_f32_e32 v222, 0xbfb8aa3b, v222
	v_mul_f32_e32 v223, 0xbfb8aa3b, v223
	v_mul_f32_e32 v224, 0xbfb8aa3b, v224
	v_mul_f32_e32 v225, 0xbfb8aa3b, v225
	v_mul_f32_e32 v226, 0xbfb8aa3b, v226
	v_mul_f32_e32 v227, 0xbfb8aa3b, v227
	v_exp_f32_e32 v220, v220
	v_exp_f32_e32 v221, v221
	v_exp_f32_e32 v222, v222
	v_exp_f32_e32 v223, v223
	v_exp_f32_e32 v224, v224
	v_exp_f32_e32 v225, v225
	v_exp_f32_e32 v226, v226
	v_exp_f32_e32 v227, v227
	v_add_f32_e32 v220, 1.0, v220
	v_add_f32_e32 v221, 1.0, v221
	v_add_f32_e32 v222, 1.0, v222
	v_add_f32_e32 v223, 1.0, v223
	v_add_f32_e32 v224, 1.0, v224
	v_add_f32_e32 v225, 1.0, v225
	v_add_f32_e32 v226, 1.0, v226
	v_add_f32_e32 v227, 1.0, v227
	v_rcp_f32_e32 v220, v220
	v_rcp_f32_e32 v221, v221
	v_rcp_f32_e32 v222, v222
	v_rcp_f32_e32 v223, v223
	v_rcp_f32_e32 v224, v224
	v_rcp_f32_e32 v225, v225
	v_rcp_f32_e32 v226, v226
	v_rcp_f32_e32 v227, v227
	v_lshlrev_b32_e32 v188, 16, v192
	v_and_b32_e32 v189, 0xffff0000, v192
	v_lshlrev_b32_e32 v190, 16, v193
	v_and_b32_e32 v191, 0xffff0000, v193
	v_pk_fma_f32 v[6:7], v[6:7], v[220:221], v[188:189]
	v_pk_fma_f32 v[8:9], v[8:9], v[222:223], v[190:191]
	v_lshlrev_b32_e32 v192, 16, v194
	v_and_b32_e32 v193, 0xffff0000, v194
	v_lshlrev_b32_e32 v194, 16, v195
	v_and_b32_e32 v195, 0xffff0000, v195
	v_pk_fma_f32 v[2:3], v[2:3], v[224:225], v[192:193]
	v_pk_fma_f32 v[4:5], v[4:5], v[226:227], v[194:195]
	v_cvt_pk_bf16_f32 v220, v6, v7
	v_cvt_pk_bf16_f32 v221, v8, v9
	v_cvt_pk_bf16_f32 v222, v2, v3
	v_cvt_pk_bf16_f32 v223, v4, v5
	global_store_dwordx4 v[150:151], v[220:223], off offset:256
	s_mov_b64 s[2:3], -1
	s_cbranch_vccnz .LBB0_1274
	s_andn2_b64 vcc, exec, s[0:1]
	s_cbranch_vccnz .LBB0_1273
	s_barrier
	s_branch .LBB0_1273
